# v32: v28 + ph2 last two column groups prefetched via recycled registers + ph6 next-unit output-gate line L2 prefetch (guarded on last unit) + ph9 modulation gain/shift/scale rolling register prefetch
# speedup vs baseline: 1.0025x; 1.0015x over previous
; __device__ __forceinline__ void ph2_norm1(const Frame& F, const Args& A) {
;     ...
;     for (int row = gw; row < S_; row += 2 * NGW) {
;         const int rowb = row + NGW < S_ ? row + NGW : row;
;         const f32x4* xa = (const f32x4*)(x + (size_t)row * DM) + F.lane; const f32x4* xb = (const f32x4*)(x + (size_t)rowb * DM) + F.lane;
;         f32x4 va[8], vb[8]; float sa = 0.f, sb = 0.f;
; #pragma unroll
;         for (int j = 0; j < 8; ++j) { va[j] = xa[64 * j]; vb[j] = xb[64 * j]; }
; #pragma unroll
;         for (int j = 0; j < 8; ++j) { sa += (va[j].x * va[j].x + va[j].y * va[j].y) + (va[j].z * va[j].z + va[j].w * va[j].w); sb += (vb[j].x * vb[j].x + vb[j].y * vb[j].y) + (vb[j].z * vb[j].z + vb[j].w * vb[j].w); }
;         const float ra = 1.f / sqrtf(wave_sum(sa) * (1.f / DM) + EPS_), rb = 1.f / sqrtf(wave_sum(sb) * (1.f / DM) + EPS_);
.LBB0_167:
	s_add_i32 s0, s16, s6
	s_cmpk_lt_i32 s0, 0x2000
	s_cselect_b32 s0, s0, s6
	global_load_dwordx4 v[30:33], v[114:115], off offset:-4096
	global_load_dwordx4 v[22:25], v[114:115], off offset:-3072
	global_load_dwordx4 v[26:29], v[114:115], off offset:-2048
	global_load_dwordx4 v[10:13], v[114:115], off offset:1024
	global_load_dwordx4 v[14:17], v[114:115], off
	global_load_dwordx4 v[18:21], v[114:115], off offset:-1024
	global_load_dwordx4 v[2:5], v[114:115], off offset:3072
	global_load_dwordx4 v[6:9], v[114:115], off offset:2048
	global_load_dwordx4 v[136:139], v[74:75], off
	v_lshl_add_u64 v[34:35], s[88:89], 0, v[118:119]
	s_ashr_i32 s1, s0, 31
	v_add_co_u32_e32 v120, vcc, s9, v34
	s_lshl_b64 s[2:3], s[0:1], 13
	s_nop 0
	v_addc_co_u32_e32 v121, vcc, 0, v35, vcc
	v_lshl_add_u64 v[34:35], v[66:67], 0, s[2:3]
	global_load_dwordx4 v[46:49], v[70:71], off
	global_load_dwordx4 v[50:53], v[72:73], off
	v_lshl_add_u64 v[36:37], s[88:89], 0, v[116:117]
	global_load_dwordx4 v[62:65], v[34:35], off offset:2048
	global_load_dwordx4 v[140:143], v[34:35], off
	global_load_dwordx4 v[144:147], v[34:35], off offset:1024
	global_load_dwordx4 v[58:61], v[34:35], off offset:3072
	v_add_co_u32_e32 v122, vcc, s18, v36
	v_mov_b32_e32 v175, 0
	s_nop 0
	v_addc_co_u32_e32 v123, vcc, 0, v37, vcc
	v_add_co_u32_e32 v34, vcc, s17, v34
	s_lshl_b64 s[20:21], s[0:1], 12
	s_nop 0
	v_addc_co_u32_e32 v35, vcc, 0, v35, vcc
	global_load_dwordx4 v[42:45], v[34:35], off offset:1024
	global_load_dwordx4 v[54:57], v[34:35], off
	global_load_dwordx4 v[38:41], v[34:35], off offset:2048
	s_nop 0
	global_load_dwordx4 v[34:37], v[34:35], off offset:3072
	global_load_dwordx4 v[188:191], v[70:71], off offset:1024
	global_load_dwordx4 v[192:195], v[80:81], off
	global_load_dwordx4 v[196:199], v[78:79], off
	global_load_dwordx4 v[200:203], v[70:71], off offset:2048
	global_load_dwordx4 v[204:207], v[84:85], off
	global_load_dwordx4 v[208:211], v[82:83], off
	global_load_dwordx4 v[212:215], v[70:71], off offset:3072
	global_load_dwordx4 v[216:219], v[88:89], off
	global_load_dwordx4 v[220:223], v[86:87], off
	global_load_dwordx4 v[224:227], v[90:91], off
	global_load_dwordx4 v[228:231], v[94:95], off
	global_load_dwordx4 v[232:235], v[92:93], off
	global_load_dwordx4 v[236:239], v[96:97], off
	global_load_dwordx4 v[240:243], v[100:101], off
	global_load_dwordx4 v[244:247], v[98:99], off
	s_lshl_b64 s[0:1], s[0:1], 11
	v_lshl_add_u64 v[124:125], v[76:77], 0, s[0:1]
	v_mov_b32_e32 v176, 0
	v_lshl_add_u64 v[126:127], v[68:69], 0, s[20:21]
	v_mov_b32_e32 v177, 0
	v_mov_b32_e32 v178, 0
	v_mov_b32_e32 v179, 0
	v_mov_b32_e32 v180, 0
	s_add_i32 s6, s6, s8
	v_lshl_add_u64 v[114:115], v[114:115], 0, s[10:11]
	v_lshl_add_u64 v[116:117], v[116:117], 0, s[12:13]
	v_lshl_add_u64 v[118:119], v[118:119], 0, s[14:15]
	s_cmpk_lt_i32 s6, 0x2000
	s_waitcnt vmcnt(33)
	v_mov_b32_e32 v150, v31
	s_waitcnt vmcnt(32)
	v_mov_b32_e32 v151, v23
	s_waitcnt vmcnt(31)
	v_pk_mul_f32 v[152:153], v[28:29], v[28:29]
	v_pk_mul_f32 v[154:155], v[26:27], v[26:27]
	s_waitcnt vmcnt(30)
	v_pk_mul_f32 v[156:157], v[12:13], v[12:13]
	v_pk_mul_f32 v[158:159], v[10:11], v[10:11]
	v_mov_b32_e32 v162, v33
	v_mov_b32_e32 v163, v25
	v_mov_b32_e32 v148, v30
	v_mov_b32_e32 v149, v22
	v_mov_b32_e32 v160, v32
	v_mov_b32_e32 v161, v24
	v_pk_mov_b32 v[170:171], v[154:155], v[152:153] op_sel:[1,0]
	v_mov_b32_e32 v155, v153
	v_pk_mov_b32 v[152:153], v[158:159], v[156:157] op_sel:[1,0]
	v_mov_b32_e32 v159, v157
	v_pk_mul_f32 v[150:151], v[150:151], v[150:151]
	v_pk_mul_f32 v[156:157], v[162:163], v[162:163]
	v_pk_fma_f32 v[148:149], v[148:149], v[148:149], v[150:151]
	v_pk_fma_f32 v[150:151], v[160:161], v[160:161], v[156:157]
	s_waitcnt vmcnt(28)
	v_mul_f32_e32 v128, v19, v19
	v_mul_f32_e32 v164, v21, v21
	s_waitcnt vmcnt(26)
	v_mul_f32_e32 v166, v7, v7
	v_mul_f32_e32 v168, v9, v9
	v_pk_add_f32 v[154:155], v[170:171], v[154:155]
	v_pk_add_f32 v[148:149], v[148:149], v[150:151]
	v_mul_f32_e32 v172, v14, v14
	v_mul_f32_e32 v173, v16, v16
	v_mul_f32_e32 v174, v17, v17
	v_mul_f32_e32 v181, v4, v4
	v_mul_f32_e32 v182, v5, v5
	v_mul_f32_e32 v183, v15, v15
	v_pk_fma_f32 v[162:163], v[18:19], v[18:19], v[128:129] op_sel_hi:[1,1,0]
	v_pk_fma_f32 v[164:165], v[20:21], v[20:21], v[164:165] op_sel_hi:[1,1,0]
	v_pk_fma_f32 v[166:167], v[6:7], v[6:7], v[166:167] op_sel_hi:[1,1,0]
	v_pk_fma_f32 v[168:169], v[8:9], v[8:9], v[168:169] op_sel_hi:[1,1,0]
	v_pk_add_f32 v[154:155], v[154:155], v[154:155] op_sel:[0,1] op_sel_hi:[1,0]
	v_pk_add_f32 v[148:149], v[148:149], v[148:149] op_sel:[0,1] op_sel_hi:[1,0]
	v_mov_b32_e32 v163, v173
	v_mov_b32_e32 v165, v174
	v_mov_b32_e32 v167, v181
	v_mov_b32_e32 v169, v182
	v_mov_b32_e32 v155, v183
	v_mov_b32_e32 v149, v172
	v_pk_add_f32 v[152:153], v[152:153], v[158:159]
	v_pk_add_f32 v[150:151], v[162:163], v[164:165]
	v_pk_add_f32 v[156:157], v[166:167], v[168:169]
	s_waitcnt vmcnt(22)
	v_pk_mul_f32 v[158:159], v[64:65], v[64:65]
	v_pk_mul_f32 v[160:161], v[62:63], v[62:63]
	v_pk_add_f32 v[148:149], v[148:149], v[154:155]
	s_waitcnt vmcnt(21)
	v_mov_b32_e32 v162, v141
	s_waitcnt vmcnt(20)
	v_mov_b32_e32 v163, v145
	v_mov_b32_e32 v166, v143
	v_mov_b32_e32 v167, v147
	v_mov_b32_e32 v154, v140
	v_mov_b32_e32 v155, v144
	v_mov_b32_e32 v164, v142
	v_mov_b32_e32 v165, v146
	v_pk_mov_b32 v[170:171], v[160:161], v[158:159] op_sel:[1,0]
	v_mov_b32_e32 v161, v159
	v_pk_add_f32 v[148:149], v[148:149], v[150:151]
	v_pk_mul_f32 v[150:151], v[162:163], v[162:163]
	v_pk_mul_f32 v[158:159], v[166:167], v[166:167]
	v_mul_f32_e32 v184, v3, v3
	v_mul_f32_e32 v185, v2, v2
	v_pk_add_f32 v[152:153], v[152:153], v[152:153] op_sel:[0,1] op_sel_hi:[1,0]
	v_pk_fma_f32 v[150:151], v[154:155], v[154:155], v[150:151]
	v_pk_fma_f32 v[154:155], v[164:165], v[164:165], v[158:159]
	v_pk_add_f32 v[148:149], v[148:149], v[148:149] op_sel:[0,1] op_sel_hi:[1,0]
	v_mov_b32_e32 v153, v184
	s_waitcnt vmcnt(19)
; __device__ __forceinline__ float wave_sum(float v) {
;     ...
;     for (int o = 1; o < 64; o <<= 1) v += __shfl_xor(v, o);
; __device__ __forceinline__ void ph2_norm1(const Frame& F, const Args& A) {
;     ...
;         for (int j = 0; j < 8; ++j) { sa += (va[j].x * va[j].x + va[j].y * va[j].y) + (va[j].z * va[j].z + va[j].w * va[j].w); sb += (vb[j].x * vb[j].x + vb[j].y * vb[j].y) + (vb[j].z * vb[j].z + vb[j].w * vb[j].w); }
;         const float ra = 1.f / sqrtf(wave_sum(sa) * (1.f / DM) + EPS_), rb = 1.f / sqrtf(wave_sum(sb) * (1.f / DM) + EPS_);
	v_mul_f32_e32 v128, v59, v59
	v_mul_f32_e32 v168, v61, v61
	v_pk_add_f32 v[158:159], v[170:171], v[160:161]
	v_pk_add_f32 v[150:151], v[150:151], v[154:155]
	v_mov_b32_e32 v149, v185
	v_pk_fma_f32 v[172:173], v[58:59], v[58:59], v[128:129] op_sel_hi:[1,1,0]
	v_pk_fma_f32 v[168:169], v[60:61], v[60:61], v[168:169] op_sel_hi:[1,1,0]
	s_waitcnt vmcnt(17)
	v_mul_f32_e32 v183, v55, v55
	v_mul_f32_e32 v184, v54, v54
	v_pk_add_f32 v[158:159], v[158:159], v[158:159] op_sel:[0,1] op_sel_hi:[1,0]
	v_pk_add_f32 v[148:149], v[148:149], v[152:153]
	v_pk_add_f32 v[150:151], v[150:151], v[150:151] op_sel:[0,1] op_sel_hi:[1,0]
	v_pk_mul_f32 v[162:163], v[44:45], v[44:45]
	v_pk_mul_f32 v[166:167], v[42:43], v[42:43]
	v_mul_f32_e32 v173, v56, v56
	v_mul_f32_e32 v169, v57, v57
	s_waitcnt vmcnt(16)
	v_mul_f32_e32 v128, v39, v39
	v_mov_b32_e32 v159, v183
	v_pk_add_f32 v[148:149], v[148:149], v[156:157]
	v_mov_b32_e32 v151, v184
	v_pk_mov_b32 v[160:161], v[166:167], v[162:163] op_sel:[1,0]
	v_mov_b32_e32 v167, v163
	v_pk_fma_f32 v[162:163], v[38:39], v[38:39], v[128:129] op_sel_hi:[1,1,0]
	v_pk_add_f32 v[154:155], v[172:173], v[168:169]
	v_pk_add_f32 v[150:151], v[150:151], v[158:159]
	v_add_f32_e32 v128, v148, v149
	v_pk_add_f32 v[148:149], v[150:151], v[154:155]
	s_nop 1
	v_mov_b32_dpp v150, v128 quad_perm:[1,0,3,2] row_mask:0xf bank_mask:0xf
	v_mul_f32_e32 v174, v41, v41
	v_pk_add_f32 v[160:161], v[160:161], v[166:167]
	s_waitcnt vmcnt(15)
	v_mul_f32_e32 v181, v36, v36
	v_mul_f32_e32 v182, v37, v37
	v_mul_f32_e32 v186, v35, v35
	v_mul_f32_e32 v187, v34, v34
	v_pk_fma_f32 v[164:165], v[40:41], v[40:41], v[174:175] op_sel_hi:[1,1,0]
	v_pk_add_f32 v[160:161], v[160:161], v[160:161] op_sel:[0,1] op_sel_hi:[1,0]
	v_pk_add_f32 v[148:149], v[148:149], v[148:149] op_sel:[0,1] op_sel_hi:[1,0]
	v_mov_b32_e32 v163, v181
	v_mov_b32_e32 v165, v182
	v_mov_b32_e32 v161, v186
	v_mov_b32_e32 v149, v187
	v_pk_add_f32 v[152:153], v[162:163], v[164:165]
	v_pk_add_f32 v[148:149], v[148:149], v[160:161]
	s_waitcnt lgkmcnt(0)
	v_add_f32_e32 v128, v128, v150
	v_pk_add_f32 v[148:149], v[148:149], v[152:153]
	v_pk_add_f32 v[138:139], v[138:139], 1.0 op_sel_hi:[1,0]
	v_add_f32_e32 v148, v148, v149
	v_mov_b32_dpp v149, v128 quad_perm:[2,3,0,1] row_mask:0xf bank_mask:0xf
	s_nop 1
	v_mov_b32_dpp v150, v148 quad_perm:[1,0,3,2] row_mask:0xf bank_mask:0xf
	v_pk_add_f32 v[136:137], v[136:137], 1.0 op_sel_hi:[1,0]
	s_waitcnt lgkmcnt(0)
	v_add_f32_e32 v128, v128, v149
	s_waitcnt lgkmcnt(0)
	v_add_f32_e32 v148, v148, v150
	ds_bpermute_b32 v149, v130, v128
	s_nop 1
	v_mov_b32_dpp v150, v148 quad_perm:[2,3,0,1] row_mask:0xf bank_mask:0xf
	s_waitcnt lgkmcnt(0)
	v_add_f32_e32 v128, v128, v149
	s_waitcnt lgkmcnt(0)
	v_add_f32_e32 v148, v148, v150
	v_mov_b32_dpp v149, v128 row_ror:8 row_mask:0xf bank_mask:0xf
	ds_bpermute_b32 v150, v130, v148
	s_waitcnt lgkmcnt(0)
	v_add_f32_e32 v128, v128, v149
	s_waitcnt lgkmcnt(0)
	v_add_f32_e32 v148, v148, v150
	ds_bpermute_b32 v149, v132, v128
	s_nop 1
	v_mov_b32_dpp v150, v148 row_ror:8 row_mask:0xf bank_mask:0xf
	s_waitcnt lgkmcnt(0)
	v_add_f32_e32 v128, v128, v149
	s_waitcnt lgkmcnt(0)
	v_add_f32_e32 v148, v148, v150
	ds_bpermute_b32 v149, v133, v128
	ds_bpermute_b32 v150, v132, v148
	s_waitcnt lgkmcnt(0)
	v_add_f32_e32 v128, v128, v149
	s_waitcnt lgkmcnt(0)
	v_add_f32_e32 v148, v148, v150
	v_fmamk_f32 v128, v128, 0x3a000000, v134
	ds_bpermute_b32 v149, v133, v148
	v_mul_f32_e32 v150, 0x4f800000, v128
	v_cmp_gt_f32_e32 vcc, s7, v128
	s_waitcnt lgkmcnt(0)
	v_add_f32_e32 v148, v148, v149
	v_cndmask_b32_e32 v128, v128, v150, vcc
	v_sqrt_f32_e32 v150, v128
	v_fmamk_f32 v148, v148, 0x3a000000, v134
	v_mul_f32_e32 v152, 0x4f800000, v148
	v_cmp_gt_f32_e64 s[0:1], s7, v148
	v_add_u32_e32 v149, -1, v150
	v_add_u32_e32 v151, 1, v150
	v_fma_f32 v153, -v149, v150, v128
	v_fma_f32 v154, -v151, v150, v128
	v_cndmask_b32_e64 v148, v148, v152, s[0:1]
	v_cmp_ge_f32_e64 s[2:3], 0, v153
	s_nop 1
	v_cndmask_b32_e64 v149, v150, v149, s[2:3]
	v_sqrt_f32_e32 v150, v148
	v_cmp_lt_f32_e64 s[2:3], 0, v154
	s_nop 1
	v_cndmask_b32_e64 v149, v149, v151, s[2:3]
	v_mul_f32_e32 v151, 0x37800000, v149
	v_cndmask_b32_e32 v149, v149, v151, vcc
	v_cmp_class_f32_e32 vcc, v128, v135
	v_add_u32_e32 v151, 1, v150
	v_fma_f32 v155, -v151, v150, v148
	v_cndmask_b32_e32 v128, v149, v128, vcc
	v_add_u32_e32 v149, -1, v150
	v_div_scale_f32 v152, s[2:3], v128, v128, 1.0
	v_fma_f32 v154, -v149, v150, v148
	v_cmp_ge_f32_e64 s[2:3], 0, v154
	v_rcp_f32_e32 v156, v152
	v_div_scale_f32 v153, vcc, 1.0, v128, 1.0
	v_cndmask_b32_e64 v149, v150, v149, s[2:3]
	v_cmp_lt_f32_e64 s[2:3], 0, v155
	s_nop 1
	v_cndmask_b32_e64 v149, v149, v151, s[2:3]
	v_mul_f32_e32 v150, 0x37800000, v149
	v_cndmask_b32_e64 v149, v149, v150, s[0:1]
	v_cmp_class_f32_e64 s[0:1], v148, v135
	v_fma_f32 v150, -v152, v156, 1.0
	v_fmac_f32_e32 v156, v150, v156
	v_cndmask_b32_e64 v157, v149, v148, s[0:1]
	v_div_scale_f32 v158, s[0:1], v157, v157, 1.0
	v_mul_f32_e32 v148, v153, v156
	v_rcp_f32_e32 v160, v158
	v_fma_f32 v149, -v152, v148, v153
	v_fmac_f32_e32 v148, v149, v156
	v_fma_f32 v149, -v152, v148, v153
	v_div_fmas_f32 v148, v149, v156, v148
	v_fma_f32 v149, -v158, v160, 1.0
	v_div_scale_f32 v159, s[0:1], 1.0, v157, 1.0
	v_fmac_f32_e32 v160, v149, v160
	v_div_fixup_f32 v128, v148, v128, 1.0
	v_mul_f32_e32 v156, v159, v160
	v_pk_mul_f32 v[32:33], v[32:33], v[128:129] op_sel_hi:[1,0]
	v_pk_mul_f32 v[30:31], v[30:31], v[128:129] op_sel_hi:[1,0]
	v_pk_mul_f32 v[154:155], v[26:27], v[128:129] op_sel_hi:[1,0]
	v_fma_f32 v26, -v158, v156, v159
	v_pk_mul_f32 v[148:149], v[24:25], v[128:129] op_sel_hi:[1,0]
	v_pk_mul_f32 v[150:151], v[22:23], v[128:129] op_sel_hi:[1,0]
; __device__ __forceinline__ unsigned pack_fp8x4(float a, float b, float c, float d) { int w = __builtin_amdgcn_cvt_pk_fp8_f32(a, b, 0, false); w = __builtin_amdgcn_cvt_pk_fp8_f32(c, d, w, true); return (unsigned)w; }
; __device__ __forceinline__ unsigned pk2(float lo, float hi) { const f32x2_t v = {lo, hi}; return __builtin_bit_cast(unsigned, __builtin_convertvector(v, bf16x2_hw)); }
; __device__ __forceinline__ void ph2_norm1(const Frame& F, const Args& A) {
;     ...
;         for (int j = 0; j < 8; ++j) { const int col = 4 * F.lane + 256 * j;
;             const f32x4 g = *(const f32x4*)(g1 + col), sh = *(const f32x4*)(MOD + col), sc = *(const f32x4*)(MOD + 2048 + col);
;             const f32x4 ha = va[j] * ra * g * (sc + 1.f) + sh, hb = vb[j] * rb * g * (sc + 1.f) + sh;
;             oa[64 * j] = (unsigned long long)pk2(ha.x, ha.y) | ((unsigned long long)pk2(ha.z, ha.w) << 32);
;             ob[64 * j] = (unsigned long long)pk2(hb.x, hb.y) | ((unsigned long long)pk2(hb.z, hb.w) << 32);
;             ((unsigned*)((unsigned char*)(A.ws + WS_XN8) + (size_t)row * DM) + F.lane)[64 * j] = pg8::pack_fp8x4(ha.x, ha.y, ha.z, ha.w);
;             ((unsigned*)((unsigned char*)(A.ws + WS_XN8) + (size_t)rowb * DM) + F.lane)[64 * j] = pg8::pack_fp8x4(hb.x, hb.y, hb.z, hb.w); }
	v_pk_mul_f32 v[22:23], v[46:47], v[30:31]
	v_pk_mul_f32 v[24:25], v[48:49], v[32:33]
	v_fmac_f32_e32 v156, v26, v160
	v_pk_fma_f32 v[24:25], v[138:139], v[24:25], v[52:53]
	v_pk_fma_f32 v[22:23], v[136:137], v[22:23], v[50:51]
	v_fma_f32 v26, -v158, v156, v159
	s_mov_b64 vcc, s[0:1]
	v_cvt_pk_fp8_f32 v175, v22, v23
	v_cvt_pk_bf16_f32 v22, v22, v23
	v_cvt_pk_bf16_f32 v23, v24, v25
	v_div_fmas_f32 v26, v26, v160, v156
	global_store_dwordx2 v[120:121], v[22:23], off
	v_div_fixup_f32 v22, v26, v157, 1.0
	v_pk_mul_f32 v[152:153], v[28:29], v[128:129] op_sel_hi:[1,0]
	v_pk_mul_f32 v[26:27], v[142:143], v[22:23] op_sel_hi:[1,0]
	v_pk_mul_f32 v[28:29], v[140:141], v[22:23] op_sel_hi:[1,0]
	v_pk_mul_f32 v[26:27], v[48:49], v[26:27]
	v_pk_mul_f32 v[28:29], v[46:47], v[28:29]
	v_cvt_pk_fp8_f32 v175, v24, v25 op_sel:[0,0,1]
	v_pk_fma_f32 v[24:25], v[138:139], v[26:27], v[52:53]
	v_pk_fma_f32 v[26:27], v[136:137], v[28:29], v[50:51]
	v_pk_mul_f32 v[32:33], v[146:147], v[22:23] op_sel_hi:[1,0]
	v_cvt_pk_fp8_f32 v176, v26, v27
	v_cvt_pk_bf16_f32 v26, v26, v27
	v_cvt_pk_bf16_f32 v27, v24, v25
	global_store_dwordx2 v[126:127], v[26:27], off
	global_store_dword v[122:123], v175, off
	v_cvt_pk_fp8_f32 v176, v24, v25 op_sel:[0,0,1]
	v_pk_mul_f32 v[140:141], v[144:145], v[22:23] op_sel_hi:[1,0]
	v_pk_mul_f32 v[18:19], v[18:19], v[128:129] op_sel_hi:[1,0]
	v_pk_mul_f32 v[20:21], v[20:21], v[128:129] op_sel_hi:[1,0]
	global_store_dword v[124:125], v176, off
	s_waitcnt vmcnt(4)
	v_mov_b64_e32 v[24:25], v[188:189]
	v_mov_b64_e32 v[26:27], v[190:191]
	v_mov_b64_e32 v[28:29], v[192:193]
	v_mov_b64_e32 v[30:31], v[194:195]
	v_mov_b64_e32 v[46:47], v[196:197]
	v_mov_b64_e32 v[48:49], v[198:199]
	global_load_dwordx4 v[188:191], v[102:103], off
	global_load_dwordx4 v[192:195], v[106:107], off
	global_load_dwordx4 v[196:199], v[104:105], off
	v_pk_mul_f32 v[14:15], v[14:15], v[128:129] op_sel_hi:[1,0]
	v_pk_mul_f32 v[16:17], v[16:17], v[128:129] op_sel_hi:[1,0]
	v_pk_mul_f32 v[10:11], v[10:11], v[128:129] op_sel_hi:[1,0]
	v_pk_mul_f32 v[12:13], v[12:13], v[128:129] op_sel_hi:[1,0]
	v_pk_mul_f32 v[6:7], v[6:7], v[128:129] op_sel_hi:[1,0]
	v_pk_mul_f32 v[8:9], v[8:9], v[128:129] op_sel_hi:[1,0]
	v_pk_mul_f32 v[2:3], v[2:3], v[128:129] op_sel_hi:[1,0]
	v_pk_mul_f32 v[4:5], v[4:5], v[128:129] op_sel_hi:[1,0]
	v_pk_mul_f32 v[50:51], v[150:151], v[24:25]
	v_pk_mul_f32 v[52:53], v[148:149], v[26:27]
	v_pk_mul_f32 v[26:27], v[32:33], v[26:27]
	v_pk_add_f32 v[30:31], v[30:31], 1.0 op_sel_hi:[1,0]
	v_pk_add_f32 v[28:29], v[28:29], 1.0 op_sel_hi:[1,0]
	v_pk_mul_f32 v[24:25], v[140:141], v[24:25]
	v_pk_fma_f32 v[32:33], v[52:53], v[30:31], v[48:49]
	v_pk_fma_f32 v[26:27], v[26:27], v[30:31], v[48:49]
	v_pk_fma_f32 v[30:31], v[50:51], v[28:29], v[46:47]
	v_pk_fma_f32 v[24:25], v[24:25], v[28:29], v[46:47]
	v_cvt_pk_fp8_f32 v177, v30, v31
	v_cvt_pk_fp8_f32 v178, v24, v25
	v_cvt_pk_bf16_f32 v28, v30, v31
	v_cvt_pk_bf16_f32 v29, v32, v33
	v_cvt_pk_fp8_f32 v177, v32, v33 op_sel:[0,0,1]
	v_cvt_pk_fp8_f32 v178, v26, v27 op_sel:[0,0,1]
	v_cvt_pk_bf16_f32 v24, v24, v25
	v_cvt_pk_bf16_f32 v25, v26, v27
	global_store_dwordx2 v[120:121], v[28:29], off offset:512
	global_store_dwordx2 v[126:127], v[24:25], off offset:512
	global_store_dword v[122:123], v177, off offset:256
	global_store_dword v[124:125], v178, off offset:256
	v_mov_b64_e32 v[24:25], v[200:201]
	v_mov_b64_e32 v[26:27], v[202:203]
	s_nop 0
	v_mov_b64_e32 v[28:29], v[204:205]
	v_mov_b64_e32 v[30:31], v[206:207]
	v_mov_b64_e32 v[46:47], v[208:209]
	v_mov_b64_e32 v[48:49], v[210:211]
	global_load_dwordx4 v[200:203], v[108:109], off
	global_load_dwordx4 v[204:207], v[112:113], off
	global_load_dwordx4 v[208:211], v[110:111], off
	v_pk_mul_f32 v[32:33], v[64:65], v[22:23] op_sel_hi:[1,0]
	v_pk_mul_f32 v[50:51], v[62:63], v[22:23] op_sel_hi:[1,0]
	v_mov_b32_e32 v23, 0
	v_pk_mul_f32 v[52:53], v[154:155], v[24:25]
	v_pk_mul_f32 v[62:63], v[152:153], v[26:27]
	v_pk_mul_f32 v[26:27], v[32:33], v[26:27]
	v_pk_add_f32 v[30:31], v[30:31], 1.0 op_sel_hi:[1,0]
	v_pk_add_f32 v[28:29], v[28:29], 1.0 op_sel_hi:[1,0]
	v_pk_mul_f32 v[24:25], v[50:51], v[24:25]
	v_pk_fma_f32 v[32:33], v[62:63], v[30:31], v[48:49]
	v_pk_fma_f32 v[26:27], v[26:27], v[30:31], v[48:49]
	v_pk_fma_f32 v[30:31], v[52:53], v[28:29], v[46:47]
	v_pk_fma_f32 v[24:25], v[24:25], v[28:29], v[46:47]
	v_cvt_pk_fp8_f32 v179, v30, v31
	v_cvt_pk_fp8_f32 v180, v24, v25
	v_cvt_pk_bf16_f32 v28, v30, v31
	v_cvt_pk_bf16_f32 v29, v32, v33
	v_cvt_pk_fp8_f32 v179, v32, v33 op_sel:[0,0,1]
	v_cvt_pk_fp8_f32 v180, v26, v27 op_sel:[0,0,1]
	v_cvt_pk_bf16_f32 v24, v24, v25
	v_cvt_pk_bf16_f32 v25, v26, v27
	global_store_dwordx2 v[120:121], v[28:29], off offset:1024
	global_store_dwordx2 v[126:127], v[24:25], off offset:1024
	global_store_dword v[122:123], v179, off offset:512
	global_store_dword v[124:125], v180, off offset:512
	v_mov_b64_e32 v[24:25], v[212:213]
	v_mov_b64_e32 v[26:27], v[214:215]
	s_nop 0
	v_mov_b64_e32 v[28:29], v[216:217]
	v_mov_b64_e32 v[30:31], v[218:219]
	v_mov_b64_e32 v[46:47], v[220:221]
	v_mov_b64_e32 v[48:49], v[222:223]
	v_pk_mul_f32 v[50:51], v[58:59], v[22:23] op_sel_hi:[1,0]
	v_mov_b32_e32 v52, 0
	v_pk_mul_f32 v[32:33], v[60:61], v[22:23] op_sel_hi:[1,0]
	v_pk_mul_f32 v[18:19], v[18:19], v[24:25]
	v_pk_add_f32 v[28:29], v[28:29], 1.0 op_sel_hi:[1,0]
	v_pk_mul_f32 v[24:25], v[50:51], v[24:25]
	v_pk_fma_f32 v[18:19], v[18:19], v[28:29], v[46:47]
	v_pk_fma_f32 v[24:25], v[24:25], v[28:29], v[46:47]
	v_cvt_pk_fp8_f32 v23, v18, v19
	v_cvt_pk_fp8_f32 v52, v24, v25
	v_pk_mul_f32 v[20:21], v[20:21], v[26:27]
	v_pk_add_f32 v[30:31], v[30:31], 1.0 op_sel_hi:[1,0]
; __device__ __forceinline__ unsigned pack_fp8x4(float a, float b, float c, float d) { int w = __builtin_amdgcn_cvt_pk_fp8_f32(a, b, 0, false); w = __builtin_amdgcn_cvt_pk_fp8_f32(c, d, w, true); return (unsigned)w; }
; __device__ __forceinline__ unsigned pk2(float lo, float hi) { const f32x2_t v = {lo, hi}; return __builtin_bit_cast(unsigned, __builtin_convertvector(v, bf16x2_hw)); }
; __device__ __forceinline__ void ph2_norm1(const Frame& F, const Args& A) {
;     ...
;         for (int j = 0; j < 8; ++j) { const int col = 4 * F.lane + 256 * j;
;             const f32x4 g = *(const f32x4*)(g1 + col), sh = *(const f32x4*)(MOD + col), sc = *(const f32x4*)(MOD + 2048 + col);
;             const f32x4 ha = va[j] * ra * g * (sc + 1.f) + sh, hb = vb[j] * rb * g * (sc + 1.f) + sh;
;             oa[64 * j] = (unsigned long long)pk2(ha.x, ha.y) | ((unsigned long long)pk2(ha.z, ha.w) << 32);
;             ob[64 * j] = (unsigned long long)pk2(hb.x, hb.y) | ((unsigned long long)pk2(hb.z, hb.w) << 32);
;             ((unsigned*)((unsigned char*)(A.ws + WS_XN8) + (size_t)row * DM) + F.lane)[64 * j] = pg8::pack_fp8x4(ha.x, ha.y, ha.z, ha.w);
;             ((unsigned*)((unsigned char*)(A.ws + WS_XN8) + (size_t)rowb * DM) + F.lane)[64 * j] = pg8::pack_fp8x4(hb.x, hb.y, hb.z, hb.w); }
	v_pk_mul_f32 v[26:27], v[32:33], v[26:27]
	v_pk_fma_f32 v[20:21], v[20:21], v[30:31], v[48:49]
	v_pk_fma_f32 v[26:27], v[26:27], v[30:31], v[48:49]
	v_cvt_pk_fp8_f32 v23, v20, v21 op_sel:[0,0,1]
	v_cvt_pk_fp8_f32 v52, v26, v27 op_sel:[0,0,1]
	v_cvt_pk_bf16_f32 v28, v18, v19
	v_cvt_pk_bf16_f32 v29, v20, v21
	v_cvt_pk_bf16_f32 v30, v24, v25
	v_cvt_pk_bf16_f32 v31, v26, v27
	global_store_dwordx2 v[120:121], v[28:29], off offset:1536
	global_store_dwordx2 v[126:127], v[30:31], off offset:1536
	global_store_dword v[122:123], v23, off offset:768
	global_store_dword v[124:125], v52, off offset:768
	v_mov_b64_e32 v[18:19], v[224:225]
	v_mov_b64_e32 v[20:21], v[226:227]
	v_mov_b64_e32 v[24:25], v[228:229]
	v_mov_b64_e32 v[26:27], v[230:231]
	s_nop 0
	v_mov_b64_e32 v[28:29], v[232:233]
	v_mov_b64_e32 v[30:31], v[234:235]
	v_mov_b32_e32 v23, 0
	v_pk_mul_f32 v[46:47], v[54:55], v[22:23] op_sel_hi:[1,0]
	v_mov_b32_e32 v48, 0
	v_pk_mul_f32 v[32:33], v[56:57], v[22:23] op_sel_hi:[1,0]
	v_pk_mul_f32 v[14:15], v[14:15], v[18:19]
	v_pk_add_f32 v[24:25], v[24:25], 1.0 op_sel_hi:[1,0]
	v_pk_mul_f32 v[18:19], v[46:47], v[18:19]
	v_pk_fma_f32 v[14:15], v[14:15], v[24:25], v[28:29]
	v_pk_fma_f32 v[18:19], v[18:19], v[24:25], v[28:29]
	v_cvt_pk_fp8_f32 v23, v14, v15
	v_cvt_pk_fp8_f32 v48, v18, v19
	v_pk_mul_f32 v[16:17], v[16:17], v[20:21]
	v_pk_add_f32 v[26:27], v[26:27], 1.0 op_sel_hi:[1,0]
	v_pk_mul_f32 v[20:21], v[32:33], v[20:21]
	v_pk_fma_f32 v[16:17], v[16:17], v[26:27], v[30:31]
	v_pk_fma_f32 v[20:21], v[20:21], v[26:27], v[30:31]
	v_cvt_pk_fp8_f32 v23, v16, v17 op_sel:[0,0,1]
	v_cvt_pk_fp8_f32 v48, v20, v21 op_sel:[0,0,1]
	v_cvt_pk_bf16_f32 v24, v14, v15
	v_cvt_pk_bf16_f32 v25, v16, v17
	v_cvt_pk_bf16_f32 v26, v18, v19
	v_cvt_pk_bf16_f32 v27, v20, v21
	global_store_dwordx2 v[120:121], v[24:25], off offset:2048
	global_store_dwordx2 v[126:127], v[26:27], off offset:2048
	global_store_dword v[122:123], v23, off offset:1024
	global_store_dword v[124:125], v48, off offset:1024
	v_mov_b64_e32 v[14:15], v[236:237]
	v_mov_b64_e32 v[16:17], v[238:239]
	v_mov_b64_e32 v[18:19], v[240:241]
	v_mov_b64_e32 v[20:21], v[242:243]
	s_nop 0
	v_mov_b64_e32 v[24:25], v[244:245]
	v_mov_b64_e32 v[26:27], v[246:247]
	v_mov_b32_e32 v23, 0
	v_pk_mul_f32 v[30:31], v[42:43], v[22:23] op_sel_hi:[1,0]
	v_mov_b32_e32 v32, 0
	v_pk_mul_f32 v[28:29], v[44:45], v[22:23] op_sel_hi:[1,0]
	v_pk_mul_f32 v[10:11], v[10:11], v[14:15]
	v_pk_add_f32 v[18:19], v[18:19], 1.0 op_sel_hi:[1,0]
	v_pk_mul_f32 v[14:15], v[30:31], v[14:15]
	v_pk_fma_f32 v[10:11], v[10:11], v[18:19], v[24:25]
	v_pk_fma_f32 v[14:15], v[14:15], v[18:19], v[24:25]
	v_cvt_pk_fp8_f32 v23, v10, v11
	v_cvt_pk_fp8_f32 v32, v14, v15
	v_pk_mul_f32 v[12:13], v[12:13], v[16:17]
	v_pk_add_f32 v[20:21], v[20:21], 1.0 op_sel_hi:[1,0]
	v_pk_mul_f32 v[16:17], v[28:29], v[16:17]
	v_pk_fma_f32 v[12:13], v[12:13], v[20:21], v[26:27]
	v_pk_fma_f32 v[16:17], v[16:17], v[20:21], v[26:27]
	v_cvt_pk_fp8_f32 v23, v12, v13 op_sel:[0,0,1]
	v_cvt_pk_fp8_f32 v32, v16, v17 op_sel:[0,0,1]
	v_cvt_pk_bf16_f32 v18, v10, v11
	v_cvt_pk_bf16_f32 v19, v12, v13
	v_cvt_pk_bf16_f32 v20, v14, v15
	v_cvt_pk_bf16_f32 v21, v16, v17
	global_store_dwordx2 v[120:121], v[18:19], off offset:2560
	global_store_dwordx2 v[126:127], v[20:21], off offset:2560
	global_store_dword v[122:123], v23, off offset:1280
	global_store_dword v[124:125], v32, off offset:1280
	s_waitcnt vmcnt(4)
	v_mov_b64_e32 v[10:11], v[188:189]
	v_mov_b64_e32 v[12:13], v[190:191]
	v_mov_b64_e32 v[14:15], v[192:193]
	v_mov_b64_e32 v[16:17], v[194:195]
	s_nop 0
	v_mov_b64_e32 v[18:19], v[196:197]
	v_mov_b64_e32 v[20:21], v[198:199]
	v_mov_b32_e32 v23, 0
	v_pk_mul_f32 v[26:27], v[38:39], v[22:23] op_sel_hi:[1,0]
	v_mov_b32_e32 v28, 0
	v_pk_mul_f32 v[24:25], v[40:41], v[22:23] op_sel_hi:[1,0]
	v_pk_mul_f32 v[6:7], v[6:7], v[10:11]
	v_pk_add_f32 v[14:15], v[14:15], 1.0 op_sel_hi:[1,0]
	v_pk_mul_f32 v[10:11], v[26:27], v[10:11]
	v_pk_fma_f32 v[6:7], v[6:7], v[14:15], v[18:19]
	v_pk_fma_f32 v[10:11], v[10:11], v[14:15], v[18:19]
	v_cvt_pk_fp8_f32 v23, v6, v7
	v_cvt_pk_fp8_f32 v28, v10, v11
	v_pk_mul_f32 v[8:9], v[8:9], v[12:13]
	v_pk_add_f32 v[16:17], v[16:17], 1.0 op_sel_hi:[1,0]
	v_pk_mul_f32 v[12:13], v[24:25], v[12:13]
	v_pk_fma_f32 v[8:9], v[8:9], v[16:17], v[20:21]
	v_pk_fma_f32 v[12:13], v[12:13], v[16:17], v[20:21]
	v_cvt_pk_fp8_f32 v23, v8, v9 op_sel:[0,0,1]
	v_cvt_pk_fp8_f32 v28, v12, v13 op_sel:[0,0,1]
	v_cvt_pk_bf16_f32 v14, v6, v7
	v_cvt_pk_bf16_f32 v15, v8, v9
	v_cvt_pk_bf16_f32 v16, v10, v11
	v_cvt_pk_bf16_f32 v17, v12, v13
	global_store_dwordx2 v[120:121], v[14:15], off offset:3072
	global_store_dwordx2 v[126:127], v[16:17], off offset:3072
	global_store_dword v[122:123], v23, off offset:1536
	global_store_dword v[124:125], v28, off offset:1536
	s_waitcnt vmcnt(4)
	v_mov_b64_e32 v[6:7], v[200:201]
	v_mov_b64_e32 v[8:9], v[202:203]
	v_mov_b64_e32 v[10:11], v[204:205]
	v_mov_b64_e32 v[12:13], v[206:207]
	s_nop 0
	v_mov_b64_e32 v[14:15], v[208:209]
	v_mov_b64_e32 v[16:17], v[210:211]
	v_mov_b32_e32 v23, 0
	v_pk_mul_f32 v[20:21], v[34:35], v[22:23] op_sel_hi:[1,0]
	v_mov_b32_e32 v24, 0
	v_pk_mul_f32 v[18:19], v[36:37], v[22:23] op_sel_hi:[1,0]
	v_pk_mul_f32 v[2:3], v[2:3], v[6:7]
	v_pk_add_f32 v[10:11], v[10:11], 1.0 op_sel_hi:[1,0]
	v_pk_mul_f32 v[6:7], v[20:21], v[6:7]
	v_pk_fma_f32 v[2:3], v[2:3], v[10:11], v[14:15]
	v_pk_fma_f32 v[6:7], v[6:7], v[10:11], v[14:15]
	v_cvt_pk_fp8_f32 v23, v2, v3
	v_cvt_pk_fp8_f32 v24, v6, v7
	v_pk_mul_f32 v[4:5], v[4:5], v[8:9]
	v_pk_add_f32 v[12:13], v[12:13], 1.0 op_sel_hi:[1,0]
	v_pk_mul_f32 v[8:9], v[18:19], v[8:9]
	v_pk_fma_f32 v[4:5], v[4:5], v[12:13], v[16:17]
	v_pk_fma_f32 v[8:9], v[8:9], v[12:13], v[16:17]
	v_cvt_pk_fp8_f32 v23, v4, v5 op_sel:[0,0,1]
	v_cvt_pk_bf16_f32 v10, v2, v3
	v_cvt_pk_bf16_f32 v11, v4, v5
	v_cvt_pk_fp8_f32 v24, v8, v9 op_sel:[0,0,1]
	v_cvt_pk_bf16_f32 v2, v6, v7
	v_cvt_pk_bf16_f32 v3, v8, v9
	global_store_dwordx2 v[120:121], v[10:11], off offset:3584
	global_store_dwordx2 v[126:127], v[2:3], off offset:3584
	global_store_dword v[122:123], v23, off offset:1792
	global_store_dword v[124:125], v24, off offset:1792
	s_cbranch_scc1 .LBB0_167

; __device__ __forceinline__ unsigned pk2(float lo, float hi) { const f32x2_t v = {lo, hi}; return __builtin_bit_cast(unsigned, __builtin_convertvector(v, bf16x2_hw)); }
; __device__ __forceinline__ float sigm(float x) { return __builtin_amdgcn_rcpf(1.f + __builtin_amdgcn_exp2f(-1.4426950408889634f * x)); }
; __device__ __forceinline__ void ph6_unit(const Frame& F, const Args& A, int c, int h) {
;     ...
;     const float r = 1.f / sqrtf((ssq[t] + ssq[64 + t] + ssq[128 + t] + ssq[192 + t]) * (1.f / 128.f) + EPS_);
;     const float* mg = A.in[I_MONG] + h * 128 + 32 * eb + 4 * hi;
;     const unsigned char* og = ws + WS_Z8 + (size_t)(t0 + t) * pg8::Z8LD + h * 128 + 32 * eb + 4 * hi;
;     bf16* hm = (bf16*)(ws + WS_HMF) + (size_t)(t0 + t) * 2048 + h * 128 + 32 * eb + 4 * hi;
; #pragma unroll
;     for (int g = 0; g < 4; ++g) { const unsigned ow = *(const unsigned*)(og + 8 * g); const f32x4 gm = *(const f32x4*)(mg + 8 * g);
;         const auto o01 = __builtin_amdgcn_cvt_pk_f32_fp8((int)ow, false), o23 = __builtin_amdgcn_cvt_pk_f32_fp8((int)ow, true);
;         uint2 pw; pw.x = pk2(o[4 * g] * r * gm.x * sigm(o01[0]), o[4 * g + 1] * r * gm.y * sigm(o01[1]));
;         pw.y = pk2(o[4 * g + 2] * r * gm.z * sigm(o23[0]), o[4 * g + 3] * r * gm.w * sigm(o23[1]));
;         *(uint2*)(hm + 8 * g) = pw; }
.LBB0_941:
	s_or_b64 exec, exec, s[50:51]
	v_or_b32_e32 v22, s0, v67
	s_waitcnt lgkmcnt(0)
	v_mov_b64_e32 v[10:11], s[56:57]
	s_movk_i32 s0, 0x1800
	v_mad_i64_i32 v[10:11], s[0:1], v22, s0, v[10:11]
	v_lshl_add_u64 v[10:11], v[10:11], 0, s[96:97]
	v_lshl_add_u64 v[10:11], v[10:11], 0, s[10:11]
	v_lshl_add_u64 v[10:11], v[10:11], 0, v[50:51]
	s_lshl_b32 s0, s96, 2
	s_mov_b32 s1, s97
	v_lshl_add_u64 v[12:13], v[52:53], 0, s[0:1]
	global_load_dword v30, v[10:11], off
	global_load_dwordx4 v[14:17], v[12:13], off
	global_load_dword v100, v[10:11], off offset:8
	global_load_dwordx4 v[104:107], v[12:13], off offset:32
	global_load_dword v101, v[10:11], off offset:16
	global_load_dwordx4 v[108:111], v[12:13], off offset:64
	global_load_dword v102, v[10:11], off offset:24
	global_load_dwordx4 v[112:115], v[12:13], off offset:96
	s_barrier
	ds_read2st64_b32 v[24:25], v80 offset0:252 offset1:253
	ds_read2st64_b32 v[26:27], v80 offset0:254 offset1:255
	s_mov_b32 s0, 0xf800000
	v_ashrrev_i32_e32 v23, 31, v22
	v_lshlrev_b64 v[22:23], 12, v[22:23]
	s_waitcnt lgkmcnt(1)
	v_add_f32_e32 v24, v24, v25
	s_waitcnt lgkmcnt(0)
	v_add_f32_e32 v24, v24, v26
	v_add_f32_e32 v24, v24, v27
	v_fmamk_f32 v24, v24, 0x3c000000, v77
	v_mul_f32_e32 v25, 0x4f800000, v24
	v_cmp_gt_f32_e32 vcc, s0, v24
	s_lshl_b32 s96, s96, 1
	v_lshl_add_u64 v[22:23], s[72:73], 0, v[22:23]
	v_cndmask_b32_e32 v24, v24, v25, vcc
	v_sqrt_f32_e32 v25, v24
	s_mov_b32 s77, s97
	v_lshl_add_u64 v[22:23], v[22:23], 0, s[96:97]
	v_mov_b32_e32 v55, v47
	v_add_u32_e32 v26, -1, v25
	v_add_u32_e32 v27, 1, v25
	v_fma_f32 v28, -v26, v25, v24
	v_fma_f32 v29, -v27, v25, v24
	v_cmp_ge_f32_e64 s[0:1], 0, v28
	v_lshl_add_u64 v[22:23], v[22:23], 0, s[76:77]
	v_lshl_add_u64 v[22:23], v[22:23], 0, v[54:55]
	v_cndmask_b32_e64 v25, v25, v26, s[0:1]
	v_cmp_lt_f32_e64 s[0:1], 0, v29
	s_add_i32 s89, s89, s92
	s_cmpk_gt_i32 s89, 0x3ff
	v_cndmask_b32_e64 v25, v25, v27, s[0:1]
	v_mul_f32_e32 v26, 0x37800000, v25
	v_cndmask_b32_e32 v25, v25, v26, vcc
	v_cmp_class_f32_e32 vcc, v24, v78
	s_nop 1
	v_cndmask_b32_e32 v24, v25, v24, vcc
	v_div_scale_f32 v25, s[0:1], v24, v24, 1.0
	v_rcp_f32_e32 v26, v25
	v_div_scale_f32 v27, vcc, 1.0, v24, 1.0
	v_fma_f32 v28, -v25, v26, 1.0
	v_fmac_f32_e32 v26, v28, v26
	v_mul_f32_e32 v28, v27, v26
	v_fma_f32 v29, -v25, v28, v27
	v_fmac_f32_e32 v28, v29, v26
	v_fma_f32 v25, -v25, v28, v27
	v_div_fmas_f32 v25, v25, v26, v28
	v_div_fixup_f32 v24, v25, v24, 1.0
	v_pk_mul_f32 v[28:29], v[58:59], v[24:25] op_sel_hi:[1,0]
	v_pk_mul_f32 v[32:33], v[60:61], v[24:25] op_sel_hi:[1,0]
	s_waitcnt vmcnt(0)
	s_cselect_b32 s98, 0, 0xc00000
	s_mov_b32 s99, 0
	v_lshl_add_u64 v[136:137], v[10:11], 0, s[98:99]
	global_load_dword v135, v[136:137], off
	v_cvt_pk_f32_fp8_e32 v[26:27], v30
	v_cvt_pk_f32_fp8_sdwa v[30:31], v30 src0_sel:WORD_1
	v_mul_f32_e32 v25, 0xbfb8aa3b, v26
	v_mul_f32_e32 v26, 0xbfb8aa3b, v27
	v_mul_f32_e32 v27, 0xbfb8aa3b, v30
	v_mul_f32_e32 v30, 0xbfb8aa3b, v31
	v_exp_f32_e32 v25, v25
	v_exp_f32_e32 v26, v26
	v_exp_f32_e32 v27, v27
	v_exp_f32_e32 v30, v30
	v_add_f32_e32 v25, 1.0, v25
	v_add_f32_e32 v31, 1.0, v26
	v_add_f32_e32 v55, 1.0, v27
	v_add_f32_e32 v58, 1.0, v30
	v_rcp_f32_e32 v26, v25
	v_rcp_f32_e32 v27, v31
	v_rcp_f32_e32 v30, v55
	v_rcp_f32_e32 v31, v58
	v_pk_mul_f32 v[14:15], v[14:15], v[28:29]
	v_pk_mul_f32 v[16:17], v[16:17], v[32:33]
	v_pk_mul_f32 v[14:15], v[14:15], v[26:27]
	v_pk_mul_f32 v[16:17], v[16:17], v[30:31]
	v_cvt_pk_bf16_f32 v14, v14, v15
	v_cvt_pk_bf16_f32 v15, v16, v17
	global_store_dwordx2 v[22:23], v[14:15], off
	v_mov_b32_e32 v25, v100
	s_nop 1
	v_mov_b64_e32 v[14:15], v[104:105]
	v_mov_b64_e32 v[16:17], v[106:107]
	v_cvt_pk_f32_fp8_e32 v[26:27], v25
	v_cvt_pk_f32_fp8_sdwa v[28:29], v25 src0_sel:WORD_1
	v_pk_mul_f32 v[18:19], v[18:19], v[24:25] op_sel_hi:[1,0]
	v_pk_mul_f32 v[20:21], v[20:21], v[24:25] op_sel_hi:[1,0]
	v_mul_f32_e32 v25, 0xbfb8aa3b, v26
	v_mul_f32_e32 v26, 0xbfb8aa3b, v27
	v_mul_f32_e32 v27, 0xbfb8aa3b, v28
	v_mul_f32_e32 v28, 0xbfb8aa3b, v29
	v_exp_f32_e32 v25, v25
	v_exp_f32_e32 v26, v26
	v_exp_f32_e32 v27, v27
	v_exp_f32_e32 v28, v28
	v_add_f32_e32 v25, 1.0, v25
	v_add_f32_e32 v29, 1.0, v26
	v_add_f32_e32 v30, 1.0, v27
	v_add_f32_e32 v31, 1.0, v28
	v_rcp_f32_e32 v26, v25
	v_rcp_f32_e32 v27, v29
	v_rcp_f32_e32 v28, v30
	v_rcp_f32_e32 v29, v31
	v_pk_mul_f32 v[14:15], v[18:19], v[14:15]
	v_pk_mul_f32 v[16:17], v[20:21], v[16:17]
	v_pk_mul_f32 v[14:15], v[14:15], v[26:27]
	v_pk_mul_f32 v[16:17], v[16:17], v[28:29]
	v_cvt_pk_bf16_f32 v14, v14, v15
	v_cvt_pk_bf16_f32 v15, v16, v17
	global_store_dwordx2 v[22:23], v[14:15], off offset:16
	v_mov_b32_e32 v20, v101
	s_nop 1
	v_mov_b64_e32 v[14:15], v[108:109]
	v_mov_b64_e32 v[16:17], v[110:111]
	v_pk_mul_f32 v[8:9], v[8:9], v[24:25] op_sel_hi:[1,0]
	v_pk_mul_f32 v[6:7], v[6:7], v[24:25] op_sel_hi:[1,0]
	v_pk_mul_f32 v[2:3], v[2:3], v[24:25] op_sel_hi:[1,0]
	v_pk_mul_f32 v[4:5], v[4:5], v[24:25] op_sel_hi:[1,0]
	v_cvt_pk_f32_fp8_e32 v[18:19], v20
	v_cvt_pk_f32_fp8_sdwa v[20:21], v20 src0_sel:WORD_1
	v_pk_mul_f32 v[8:9], v[8:9], v[14:15]
	v_pk_mul_f32 v[6:7], v[6:7], v[16:17]
	v_mul_f32_e32 v18, 0xbfb8aa3b, v18
	v_mul_f32_e32 v19, 0xbfb8aa3b, v19
	v_mul_f32_e32 v20, 0xbfb8aa3b, v20
	v_mul_f32_e32 v21, 0xbfb8aa3b, v21
	v_exp_f32_e32 v18, v18
	v_exp_f32_e32 v19, v19
	v_exp_f32_e32 v20, v20
	v_exp_f32_e32 v21, v21
	v_add_f32_e32 v18, 1.0, v18
	v_add_f32_e32 v19, 1.0, v19
	v_add_f32_e32 v20, 1.0, v20
	v_add_f32_e32 v21, 1.0, v21
	v_rcp_f32_e32 v18, v18
	v_rcp_f32_e32 v19, v19
	v_rcp_f32_e32 v20, v20
	v_rcp_f32_e32 v21, v21
	v_pk_mul_f32 v[8:9], v[8:9], v[18:19]
	s_nop 0
	v_cvt_pk_bf16_f32 v8, v8, v9
	v_pk_mul_f32 v[6:7], v[6:7], v[20:21]
	s_nop 0
	v_cvt_pk_bf16_f32 v9, v6, v7
	global_store_dwordx2 v[22:23], v[8:9], off offset:32
	v_mov_b32_e32 v14, v102
	s_nop 1
	v_mov_b64_e32 v[6:7], v[112:113]
	v_mov_b64_e32 v[8:9], v[114:115]
	v_cvt_pk_f32_fp8_e32 v[10:11], v14
	v_cvt_pk_f32_fp8_sdwa v[12:13], v14 src0_sel:WORD_1
	v_pk_mul_f32 v[2:3], v[2:3], v[6:7]
	v_pk_mul_f32 v[4:5], v[4:5], v[8:9]
	v_mul_f32_e32 v10, 0xbfb8aa3b, v10
	v_mul_f32_e32 v11, 0xbfb8aa3b, v11
	v_mul_f32_e32 v12, 0xbfb8aa3b, v12
	v_mul_f32_e32 v13, 0xbfb8aa3b, v13
	v_exp_f32_e32 v10, v10
	v_exp_f32_e32 v11, v11
	v_exp_f32_e32 v12, v12
	v_exp_f32_e32 v13, v13
	v_add_f32_e32 v10, 1.0, v10
	v_add_f32_e32 v11, 1.0, v11
	v_add_f32_e32 v12, 1.0, v12
	v_add_f32_e32 v13, 1.0, v13
	v_rcp_f32_e32 v10, v10
	v_rcp_f32_e32 v11, v11
	v_rcp_f32_e32 v12, v12
	v_rcp_f32_e32 v13, v13
	v_pk_mul_f32 v[2:3], v[2:3], v[10:11]
	s_nop 0
	v_cvt_pk_bf16_f32 v2, v2, v3
	v_pk_mul_f32 v[4:5], v[4:5], v[12:13]
	s_nop 0
	v_cvt_pk_bf16_f32 v3, v4, v5
	global_store_dwordx2 v[22:23], v[2:3], off offset:48
	s_barrier
	s_cbranch_scc1 .LBB0_968

; __device__ __forceinline__ void ph9_router(const Frame& F, const Args& A) {
;     ...
;     for (int grp = F.vcu; grp < S_ / 32; grp += F.G) {
;         int lane = F.lane; asm volatile("" : "+v"(lane));
;         const int tid = F.wave * 64 + lane;
;         const int r0 = grp * 32 + F.wave * 4;
;         if (tid < 32) cntL[tid] = 0u;
;         f32x4 hv[4][8];
;         { f32x4 t16[16];
; #pragma unroll
;           for (int i = 0; i < 16; ++i) t16[i] = ((const f32x4*)WRT)[tid + 512 * i];
;           __builtin_amdgcn_sched_barrier(0);
; #pragma unroll
;           for (int r = 0; r < 4; ++r) { const f32x4* xr = (const f32x4*)(X1 + (size_t)(r0 + r) * DM) + lane;
; #pragma unroll
;               for (int j = 0; j < 8; ++j) hv[r][j] = xr[64 * j]; }
;           __builtin_amdgcn_sched_barrier(0);
; #pragma unroll
;           for (int i = 0; i < 16; ++i) wl[tid + 512 * i] = t16[i]; }
.LBB0_1193:
	v_mov_b32_e32 v132, v1
	s_nop 0
	v_add_u32_e32 v134, s44, v132
	v_cmp_gt_i32_e64 s[2:3], 32, v134
	v_lshl_add_u32 v192, v134, 2, 0
	s_and_saveexec_b64 s[0:1], s[2:3]
	v_add_u32_e32 v2, 0x20500, v192
	ds_write_b32 v2, v131
	s_or_b64 exec, exec, s[0:1]
	v_ashrrev_i32_e32 v135, 31, v134
	v_lshl_add_u64 v[2:3], v[134:135], 4, s[20:21]
	v_add_co_u32_e32 v4, vcc, 0x2000, v2
	s_lshl_b32 s0, s52, 5
	s_nop 0
	v_addc_co_u32_e32 v5, vcc, 0, v3, vcc
	global_load_dwordx4 v[136:139], v[2:3], off
	global_load_dwordx4 v[140:143], v[4:5], off
	v_add_co_u32_e32 v4, vcc, 0x4000, v2
	s_add_i32 s40, s0, s45
	s_nop 0
	v_addc_co_u32_e32 v5, vcc, 0, v3, vcc
	v_add_co_u32_e32 v6, vcc, 0x6000, v2
	s_mov_b32 s42, 0
	s_nop 0
	v_addc_co_u32_e32 v7, vcc, 0, v3, vcc
	global_load_dwordx4 v[144:147], v[4:5], off
	global_load_dwordx4 v[148:151], v[6:7], off
	v_add_co_u32_e32 v4, vcc, 0x8000, v2
	s_nop 1
	v_addc_co_u32_e32 v5, vcc, 0, v3, vcc
	v_add_co_u32_e32 v6, vcc, 0xa000, v2
	s_nop 1
	v_addc_co_u32_e32 v7, vcc, 0, v3, vcc
	global_load_dwordx4 v[152:155], v[4:5], off
	global_load_dwordx4 v[156:159], v[6:7], off
	v_add_co_u32_e32 v4, vcc, 0xc000, v2
	s_nop 1
	v_addc_co_u32_e32 v5, vcc, 0, v3, vcc
	v_add_co_u32_e32 v6, vcc, 0xe000, v2
	s_nop 1
	v_addc_co_u32_e32 v7, vcc, 0, v3, vcc
	global_load_dwordx4 v[160:163], v[4:5], off
	global_load_dwordx4 v[164:167], v[6:7], off
	v_add_co_u32_e32 v4, vcc, 0x10000, v2
	s_nop 1
	v_addc_co_u32_e32 v5, vcc, 0, v3, vcc
	v_add_co_u32_e32 v6, vcc, 0x12000, v2
	s_nop 1
	v_addc_co_u32_e32 v7, vcc, 0, v3, vcc
	global_load_dwordx4 v[174:177], v[4:5], off
	global_load_dwordx4 v[194:197], v[6:7], off
	v_add_co_u32_e32 v4, vcc, 0x14000, v2
	s_nop 1
	v_addc_co_u32_e32 v5, vcc, 0, v3, vcc
	v_add_co_u32_e32 v6, vcc, 0x16000, v2
	s_nop 1
	v_addc_co_u32_e32 v7, vcc, 0, v3, vcc
	global_load_dwordx4 v[198:201], v[4:5], off
	global_load_dwordx4 v[202:205], v[6:7], off
	v_add_co_u32_e32 v4, vcc, 0x18000, v2
	s_nop 1
	v_addc_co_u32_e32 v5, vcc, 0, v3, vcc
	v_add_co_u32_e32 v6, vcc, 0x1a000, v2
	s_nop 1
	v_addc_co_u32_e32 v7, vcc, 0, v3, vcc
	global_load_dwordx4 v[206:209], v[4:5], off
	global_load_dwordx4 v[210:213], v[6:7], off
	v_add_co_u32_e32 v4, vcc, 0x1c000, v2
	s_nop 1
	v_addc_co_u32_e32 v5, vcc, 0, v3, vcc
	v_add_co_u32_e32 v2, vcc, 0x1e000, v2
	s_nop 1
	v_addc_co_u32_e32 v3, vcc, 0, v3, vcc
	global_load_dwordx4 v[214:217], v[4:5], off
	global_load_dwordx4 v[218:221], v[2:3], off
	v_readlane_b32 s4, v254, 33
	v_ashrrev_i32_e32 v133, 31, v132
	v_readlane_b32 s5, v254, 34
	s_ashr_i32 s41, s40, 31
	v_readlane_b32 s6, v254, 35
	v_lshl_add_u64 v[2:3], v[132:133], 4, s[4:5]
	s_lshl_b64 s[0:1], s[40:41], 13
	v_readlane_b32 s7, v254, 36
	v_lshl_add_u64 v[4:5], v[2:3], 0, s[0:1]
	s_or_b32 s6, s40, 1
	global_load_dwordx4 v[114:117], v[4:5], off
	global_load_dwordx4 v[102:105], v[4:5], off offset:1024
	global_load_dwordx4 v[94:97], v[4:5], off offset:2048
	global_load_dwordx4 v[90:93], v[4:5], off offset:3072
	v_add_co_u32_e32 v4, vcc, s46, v4
	s_ashr_i32 s7, s6, 31
	s_nop 0
	v_addc_co_u32_e32 v5, vcc, 0, v5, vcc
	s_lshl_b64 s[0:1], s[6:7], 13
	global_load_dwordx4 v[122:125], v[4:5], off
	global_load_dwordx4 v[118:121], v[4:5], off offset:1024
	global_load_dwordx4 v[106:109], v[4:5], off offset:2048
	global_load_dwordx4 v[98:101], v[4:5], off offset:3072
	v_lshl_add_u64 v[4:5], v[2:3], 0, s[0:1]
	s_or_b32 s4, s40, 2
	global_load_dwordx4 v[126:129], v[4:5], off
	global_load_dwordx4 v[110:113], v[4:5], off offset:1024
	global_load_dwordx4 v[86:89], v[4:5], off offset:2048
	global_load_dwordx4 v[82:85], v[4:5], off offset:3072
	v_add_co_u32_e32 v4, vcc, s46, v4
	s_ashr_i32 s5, s4, 31
	s_nop 0
	v_addc_co_u32_e32 v5, vcc, 0, v5, vcc
	s_lshl_b64 s[0:1], s[4:5], 13
	global_load_dwordx4 v[78:81], v[4:5], off
	global_load_dwordx4 v[74:77], v[4:5], off offset:1024
	global_load_dwordx4 v[70:73], v[4:5], off offset:2048
	global_load_dwordx4 v[62:65], v[4:5], off offset:3072
	v_lshl_add_u64 v[4:5], v[2:3], 0, s[0:1]
	s_or_b32 s0, s40, 3
	v_readlane_b32 s8, v254, 37
	v_readlane_b32 s9, v254, 38
	s_ashr_i32 s1, s0, 31
	global_load_dwordx4 v[66:69], v[4:5], off
	global_load_dwordx4 v[58:61], v[4:5], off offset:1024
	global_load_dwordx4 v[54:57], v[4:5], off offset:2048
	global_load_dwordx4 v[50:53], v[4:5], off offset:3072
	v_add_co_u32_e32 v4, vcc, s46, v4
	s_lshl_b64 s[8:9], s[0:1], 13
	s_nop 0
	v_addc_co_u32_e32 v5, vcc, 0, v5, vcc
	v_lshl_add_u64 v[2:3], v[2:3], 0, s[8:9]
	global_load_dwordx4 v[46:49], v[4:5], off
	global_load_dwordx4 v[42:45], v[4:5], off offset:1024
	global_load_dwordx4 v[38:41], v[4:5], off offset:2048
	global_load_dwordx4 v[34:37], v[4:5], off offset:3072
	global_load_dwordx4 v[30:33], v[2:3], off
	global_load_dwordx4 v[26:29], v[2:3], off offset:1024
	global_load_dwordx4 v[22:25], v[2:3], off offset:2048
	global_load_dwordx4 v[18:21], v[2:3], off offset:3072
	v_add_co_u32_e32 v2, vcc, s46, v2
	v_readlane_b32 s10, v254, 39
	s_nop 0
	v_addc_co_u32_e32 v3, vcc, 0, v3, vcc
	global_load_dwordx4 v[14:17], v[2:3], off
	global_load_dwordx4 v[10:13], v[2:3], off offset:1024
	global_load_dwordx4 v[6:9], v[2:3], off offset:2048
	s_nop 0
	global_load_dwordx4 v[2:5], v[2:3], off offset:3072
	v_readlane_b32 s11, v254, 40
	v_readlane_b32 s12, v254, 41
	v_readlane_b32 s13, v254, 42
	v_readlane_b32 s14, v254, 43
	v_readlane_b32 s15, v254, 44
	v_readlane_b32 s16, v254, 45
	v_readlane_b32 s17, v254, 46
	v_readlane_b32 s18, v254, 47
	v_readlane_b32 s19, v254, 48
	v_lshl_add_u32 v135, v134, 4, 0
	v_add_u32_e32 v130, 0x10000, v135
	s_waitcnt vmcnt(47)
	ds_write_b128 v135, v[136:139]
	s_waitcnt vmcnt(46)
	ds_write_b128 v135, v[140:143] offset:8192
	s_waitcnt vmcnt(45)
; __device__ __forceinline__ void ph9_router(const Frame& F, const Args& A) {
;     ...
;           for (int i = 0; i < 16; ++i) wl[tid + 512 * i] = t16[i]; }
;         __builtin_amdgcn_sched_barrier(0);
; #pragma unroll
;         for (int r = 0; r < 4; ++r) { const uint2* dr = (const uint2*)(DX + (size_t)(r0 + r) * DM) + lane; uint2 dw[8];
; #pragma unroll
;             for (int j = 0; j < 8; ++j) dw[j] = dr[64 * j];
; #pragma unroll
;             for (int j = 0; j < 8; ++j) { hv[r][j].x += bflo(dw[j].x); hv[r][j].y += bfhi(dw[j].x); hv[r][j].z += bflo(dw[j].y); hv[r][j].w += bfhi(dw[j].y); } }
	ds_write_b128 v135, v[144:147] offset:16384
	s_waitcnt vmcnt(44)
	ds_write_b128 v135, v[148:151] offset:24576
	s_waitcnt vmcnt(43)
	ds_write_b128 v135, v[152:155] offset:32768
	s_waitcnt vmcnt(42)
	ds_write_b128 v135, v[156:159] offset:40960
	s_waitcnt vmcnt(41)
	ds_write_b128 v135, v[160:163] offset:49152
	s_waitcnt vmcnt(40)
	ds_write_b128 v135, v[164:167] offset:57344
	s_waitcnt vmcnt(39)
	ds_write_b128 v130, v[174:177]
	v_add_u32_e32 v130, 0x12000, v135
	s_waitcnt vmcnt(38)
	ds_write_b128 v130, v[194:197]
	v_add_u32_e32 v130, 0x14000, v135
	s_waitcnt vmcnt(37)
	ds_write_b128 v130, v[198:201]
	v_add_u32_e32 v130, 0x16000, v135
	s_waitcnt vmcnt(36)
	ds_write_b128 v130, v[202:205]
	v_add_u32_e32 v130, 0x18000, v135
	s_waitcnt vmcnt(35)
	ds_write_b128 v130, v[206:209]
	v_add_u32_e32 v130, 0x1a000, v135
	s_waitcnt vmcnt(34)
	ds_write_b128 v130, v[210:213]
	v_add_u32_e32 v130, 0x1c000, v135
	s_waitcnt vmcnt(33)
	ds_write_b128 v130, v[214:217]
	v_add_u32_e32 v130, 0x1e000, v135
	s_waitcnt vmcnt(32)
	ds_write_b128 v130, v[218:221]
	v_lshl_add_u64 v[136:137], v[132:133], 3, s[58:59]
	s_lshl_b64 s[8:9], s[40:41], 12
	v_lshl_add_u64 v[138:139], v[136:137], 0, s[8:9]
	global_load_dwordx2 v[140:141], v[138:139], off
	global_load_dwordx2 v[142:143], v[138:139], off offset:512
	global_load_dwordx2 v[144:145], v[138:139], off offset:1024
	global_load_dwordx2 v[146:147], v[138:139], off offset:1536
	global_load_dwordx2 v[148:149], v[138:139], off offset:2048
	global_load_dwordx2 v[150:151], v[138:139], off offset:2560
	global_load_dwordx2 v[152:153], v[138:139], off offset:3072
	s_nop 0
	global_load_dwordx2 v[138:139], v[138:139], off offset:3584
	s_lshl_b64 s[6:7], s[6:7], 12
	v_lshl_add_u64 v[154:155], v[136:137], 0, s[6:7]
	global_load_dwordx2 v[156:157], v[154:155], off
	global_load_dwordx2 v[164:165], v[154:155], off offset:512
	global_load_dwordx2 v[166:167], v[154:155], off offset:1024
	global_load_dwordx2 v[174:175], v[154:155], off offset:1536
	s_lshl_b64 s[4:5], s[4:5], 12
	v_lshl_add_u64 v[176:177], v[136:137], 0, s[4:5]
	global_load_dwordx2 v[178:179], v[154:155], off offset:2048
	global_load_dwordx2 v[194:195], v[154:155], off offset:2560
	global_load_dwordx2 v[196:197], v[154:155], off offset:3072
	global_load_dwordx2 v[198:199], v[154:155], off offset:3584
	global_load_dwordx2 v[200:201], v[176:177], off
	global_load_dwordx2 v[202:203], v[176:177], off offset:512
	global_load_dwordx2 v[204:205], v[176:177], off offset:1024
	global_load_dwordx2 v[206:207], v[176:177], off offset:1536
	global_load_dwordx2 v[208:209], v[176:177], off offset:2048
	s_lshl_b64 s[0:1], s[0:1], 12
	v_cmp_lt_i32_e32 vcc, v182, v181
	s_waitcnt vmcnt(20)
	v_lshlrev_b32_e32 v154, 16, v140
	s_waitcnt vmcnt(19)
	v_lshlrev_b32_e32 v160, 16, v142
	v_and_b32_e32 v161, 0xffff0000, v142
	v_lshlrev_b32_e32 v142, 16, v143
	v_and_b32_e32 v143, 0xffff0000, v143
	s_waitcnt vmcnt(17)
	v_lshlrev_b32_e32 v210, 16, v146
	v_and_b32_e32 v211, 0xffff0000, v146
	s_waitcnt vmcnt(15)
	v_lshlrev_b32_e32 v218, 16, v150
	v_and_b32_e32 v219, 0xffff0000, v150
	v_lshlrev_b32_e32 v214, 16, v148
	v_and_b32_e32 v215, 0xffff0000, v148
	v_lshlrev_b32_e32 v216, 16, v149
	v_and_b32_e32 v217, 0xffff0000, v149
	v_pk_add_f32 v[148:149], v[104:105], v[142:143]
	v_pk_add_f32 v[104:105], v[90:91], v[210:211]
	v_pk_add_f32 v[90:91], v[118:119], v[218:219]
	global_load_dwordx2 v[118:119], v[176:177], off offset:2560
	v_and_b32_e32 v155, 0xffff0000, v140
	v_lshlrev_b32_e32 v140, 16, v141
	v_and_b32_e32 v141, 0xffff0000, v141
	v_lshlrev_b32_e32 v212, 16, v147
	v_and_b32_e32 v213, 0xffff0000, v147
	v_lshlrev_b32_e32 v150, 16, v151
	v_and_b32_e32 v151, 0xffff0000, v151
	v_pk_add_f32 v[158:159], v[116:117], v[140:141]
	v_pk_add_f32 v[116:117], v[92:93], v[212:213]
	v_pk_add_f32 v[92:93], v[120:121], v[150:151]
	global_load_dwordx2 v[120:121], v[176:177], off offset:3072
	s_waitcnt vmcnt(15)
	v_lshlrev_b32_e32 v222, 16, v138
	v_and_b32_e32 v223, 0xffff0000, v138
	s_waitcnt vmcnt(14)
	v_lshlrev_b32_e32 v224, 16, v156
	v_and_b32_e32 v225, 0xffff0000, v156
	v_lshlrev_b32_e32 v226, 16, v157
	v_and_b32_e32 v227, 0xffff0000, v157
	v_pk_add_f32 v[156:157], v[114:115], v[154:155]
	v_pk_add_f32 v[114:115], v[98:99], v[222:223]
	s_waitcnt vmcnt(13)
	v_lshlrev_b32_e32 v98, 16, v165
	v_and_b32_e32 v99, 0xffff0000, v165
	v_lshlrev_b32_e32 v162, 16, v144
	v_and_b32_e32 v163, 0xffff0000, v144
	v_lshlrev_b32_e32 v144, 16, v145
	v_and_b32_e32 v145, 0xffff0000, v145
	v_lshlrev_b32_e32 v138, 16, v139
	v_and_b32_e32 v139, 0xffff0000, v139
	v_pk_add_f32 v[154:155], v[112:113], v[98:99]
	s_waitcnt vmcnt(12)
	v_lshlrev_b32_e32 v98, 16, v166
	v_and_b32_e32 v99, 0xffff0000, v166
	v_lshlrev_b32_e32 v220, 16, v152
	v_and_b32_e32 v221, 0xffff0000, v152
	v_lshlrev_b32_e32 v152, 16, v153
	v_and_b32_e32 v153, 0xffff0000, v153
	v_pk_add_f32 v[140:141], v[94:95], v[162:163]
	v_pk_add_f32 v[142:143], v[96:97], v[144:145]
	v_pk_add_f32 v[96:97], v[122:123], v[214:215]
	v_pk_add_f32 v[122:123], v[100:101], v[138:139]
	v_pk_add_f32 v[162:163], v[128:129], v[226:227]
	v_pk_add_f32 v[128:129], v[86:87], v[98:99]
	v_lshlrev_b32_e32 v86, 16, v167
	v_and_b32_e32 v87, 0xffff0000, v167
	global_load_dwordx2 v[138:139], v[176:177], off offset:3584
	v_pk_add_f32 v[94:95], v[106:107], v[220:221]
	v_pk_add_f32 v[106:107], v[108:109], v[152:153]
	v_pk_add_f32 v[144:145], v[88:89], v[86:87]
	s_waitcnt vmcnt(12)
	v_lshlrev_b32_e32 v86, 16, v174
	v_and_b32_e32 v87, 0xffff0000, v174
	v_lshl_add_u64 v[152:153], v[136:137], 0, s[0:1]
	v_lshlrev_b32_e32 v228, 16, v164
	v_and_b32_e32 v229, 0xffff0000, v164
	v_pk_add_f32 v[86:87], v[82:83], v[86:87]
	v_lshlrev_b32_e32 v82, 16, v175
	v_and_b32_e32 v83, 0xffff0000, v175
	global_load_dwordx2 v[164:165], v[152:153], off
	global_load_dwordx2 v[166:167], v[152:153], off offset:512
	v_pk_add_f32 v[88:89], v[84:85], v[82:83]
	s_waitcnt vmcnt(13)
; __device__ __forceinline__ void ph9_router(const Frame& F, const Args& A) {
;     ...
;         for (int r = 0; r < 4; ++r) { const uint2* dr = (const uint2*)(DX + (size_t)(r0 + r) * DM) + lane; uint2 dw[8];
; #pragma unroll
;             for (int j = 0; j < 8; ++j) dw[j] = dr[64 * j];
; #pragma unroll
;             for (int j = 0; j < 8; ++j) { hv[r][j].x += bflo(dw[j].x); hv[r][j].y += bfhi(dw[j].x); hv[r][j].z += bflo(dw[j].y); hv[r][j].w += bfhi(dw[j].y); } }
	v_lshlrev_b32_e32 v82, 16, v178
	v_and_b32_e32 v83, 0xffff0000, v178
	v_pk_add_f32 v[78:79], v[78:79], v[82:83]
	v_lshlrev_b32_e32 v82, 16, v179
	v_and_b32_e32 v83, 0xffff0000, v179
	v_pk_add_f32 v[100:101], v[80:81], v[82:83]
	s_waitcnt vmcnt(12)
	v_lshlrev_b32_e32 v80, 16, v194
	v_and_b32_e32 v81, 0xffff0000, v194
	v_pk_add_f32 v[82:83], v[74:75], v[80:81]
	v_lshlrev_b32_e32 v74, 16, v195
	global_load_dwordx2 v[80:81], v[152:153], off offset:1024
	v_and_b32_e32 v75, 0xffff0000, v195
	v_pk_add_f32 v[84:85], v[76:77], v[74:75]
	s_waitcnt vmcnt(12)
	v_lshlrev_b32_e32 v74, 16, v196
	v_and_b32_e32 v75, 0xffff0000, v196
	v_pk_add_f32 v[98:99], v[70:71], v[74:75]
	global_load_dwordx2 v[74:75], v[152:153], off offset:1536
	global_load_dwordx2 v[76:77], v[152:153], off offset:2048
	global_load_dwordx2 v[174:175], v[152:153], off offset:2560
	v_lshlrev_b32_e32 v70, 16, v197
	v_and_b32_e32 v71, 0xffff0000, v197
	v_pk_add_f32 v[108:109], v[72:73], v[70:71]
	s_waitcnt vmcnt(14)
	v_lshlrev_b32_e32 v70, 16, v198
	v_and_b32_e32 v71, 0xffff0000, v198
	v_pk_add_f32 v[150:151], v[110:111], v[228:229]
	v_pk_add_f32 v[110:111], v[62:63], v[70:71]
	v_lshlrev_b32_e32 v62, 16, v199
	v_and_b32_e32 v63, 0xffff0000, v199
	v_pk_add_f32 v[146:147], v[102:103], v[160:161]
	v_pk_add_f32 v[102:103], v[124:125], v[216:217]
	v_pk_add_f32 v[124:125], v[64:65], v[62:63]
	s_waitcnt vmcnt(13)
	v_lshlrev_b32_e32 v62, 16, v200
	v_and_b32_e32 v63, 0xffff0000, v200
	v_pk_add_f32 v[72:73], v[66:67], v[62:63]
	v_lshlrev_b32_e32 v62, 16, v201
	v_and_b32_e32 v63, 0xffff0000, v201
	v_pk_add_f32 v[68:69], v[68:69], v[62:63]
	s_waitcnt vmcnt(12)
	v_lshlrev_b32_e32 v62, 16, v202
	v_and_b32_e32 v63, 0xffff0000, v202
	v_pk_add_f32 v[62:63], v[58:59], v[62:63]
	v_lshlrev_b32_e32 v58, 16, v203
	v_and_b32_e32 v59, 0xffff0000, v203
	v_pk_add_f32 v[64:65], v[60:61], v[58:59]
	s_waitcnt vmcnt(11)
	v_lshlrev_b32_e32 v58, 16, v204
	v_and_b32_e32 v59, 0xffff0000, v204
	v_pk_add_f32 v[54:55], v[54:55], v[58:59]
	v_lshlrev_b32_e32 v58, 16, v205
	v_and_b32_e32 v59, 0xffff0000, v205
	v_pk_add_f32 v[56:57], v[56:57], v[58:59]
	s_waitcnt vmcnt(10)
	v_lshlrev_b32_e32 v58, 16, v206
	v_and_b32_e32 v59, 0xffff0000, v206
	v_pk_add_f32 v[50:51], v[50:51], v[58:59]
	v_lshlrev_b32_e32 v58, 16, v207
	v_and_b32_e32 v59, 0xffff0000, v207
	v_pk_add_f32 v[58:59], v[52:53], v[58:59]
	s_waitcnt vmcnt(9)
	v_lshlrev_b32_e32 v52, 16, v208
	v_and_b32_e32 v53, 0xffff0000, v208
	v_pk_add_f32 v[66:67], v[46:47], v[52:53]
	v_lshlrev_b32_e32 v46, 16, v209
	v_and_b32_e32 v47, 0xffff0000, v209
	v_pk_add_f32 v[70:71], v[48:49], v[46:47]
	s_waitcnt vmcnt(8)
	v_lshlrev_b32_e32 v46, 16, v118
	v_and_b32_e32 v47, 0xffff0000, v118
	v_pk_add_f32 v[112:113], v[42:43], v[46:47]
	v_lshlrev_b32_e32 v42, 16, v119
	v_and_b32_e32 v43, 0xffff0000, v119
	v_pk_add_f32 v[160:161], v[126:127], v[224:225]
	v_pk_add_f32 v[126:127], v[44:45], v[42:43]
	s_waitcnt vmcnt(7)
	v_lshlrev_b32_e32 v42, 16, v120
	v_and_b32_e32 v43, 0xffff0000, v120
	v_pk_add_f32 v[118:119], v[38:39], v[42:43]
	global_load_dwordx2 v[44:45], v[152:153], off offset:3072
	global_load_dwordx2 v[42:43], v[152:153], off offset:3584
	v_lshlrev_b32_e32 v38, 16, v121
	v_and_b32_e32 v39, 0xffff0000, v121
	v_pk_add_f32 v[120:121], v[40:41], v[38:39]
	s_waitcnt vmcnt(8)
	v_lshlrev_b32_e32 v38, 16, v138
	v_and_b32_e32 v39, 0xffff0000, v138
	v_pk_add_f32 v[136:137], v[34:35], v[38:39]
	v_lshlrev_b32_e32 v34, 16, v139
	v_and_b32_e32 v35, 0xffff0000, v139
	v_pk_add_f32 v[138:139], v[36:37], v[34:35]
	s_waitcnt vmcnt(7)
	v_lshlrev_b32_e32 v34, 16, v164
	v_and_b32_e32 v35, 0xffff0000, v164
	v_pk_add_f32 v[38:39], v[30:31], v[34:35]
	v_lshlrev_b32_e32 v30, 16, v165
	v_and_b32_e32 v31, 0xffff0000, v165
	v_pk_add_f32 v[40:41], v[32:33], v[30:31]
	s_waitcnt vmcnt(6)
	v_lshlrev_b32_e32 v30, 16, v166
	v_and_b32_e32 v31, 0xffff0000, v166
	v_pk_add_f32 v[32:33], v[26:27], v[30:31]
	v_lshlrev_b32_e32 v26, 16, v167
	v_and_b32_e32 v27, 0xffff0000, v167
	v_pk_add_f32 v[28:29], v[28:29], v[26:27]
	s_waitcnt vmcnt(5)
	v_lshlrev_b32_e32 v26, 16, v80
	v_and_b32_e32 v27, 0xffff0000, v80
	v_pk_add_f32 v[34:35], v[22:23], v[26:27]
	v_lshlrev_b32_e32 v22, 16, v81
	v_and_b32_e32 v23, 0xffff0000, v81
	v_pk_add_f32 v[36:37], v[24:25], v[22:23]
	s_waitcnt vmcnt(4)
	v_lshlrev_b32_e32 v22, 16, v74
	v_and_b32_e32 v23, 0xffff0000, v74
	v_pk_add_f32 v[46:47], v[18:19], v[22:23]
	v_lshlrev_b32_e32 v18, 16, v75
	v_and_b32_e32 v19, 0xffff0000, v75
	v_pk_add_f32 v[60:61], v[20:21], v[18:19]
	s_waitcnt vmcnt(3)
	v_lshlrev_b32_e32 v18, 16, v76
	v_and_b32_e32 v19, 0xffff0000, v76
	v_pk_add_f32 v[74:75], v[14:15], v[18:19]
	v_lshlrev_b32_e32 v14, 16, v77
	v_and_b32_e32 v15, 0xffff0000, v77
	v_pk_add_f32 v[164:165], v[16:17], v[14:15]
	s_waitcnt vmcnt(2)
; __device__ __forceinline__ void ph9_router(const Frame& F, const Args& A) {
;     ...
;         for (int r = 0; r < 4; ++r) { const uint2* dr = (const uint2*)(DX + (size_t)(r0 + r) * DM) + lane; uint2 dw[8];
; #pragma unroll
;             for (int j = 0; j < 8; ++j) dw[j] = dr[64 * j];
; #pragma unroll
;             for (int j = 0; j < 8; ++j) { hv[r][j].x += bflo(dw[j].x); hv[r][j].y += bfhi(dw[j].x); hv[r][j].z += bflo(dw[j].y); hv[r][j].w += bfhi(dw[j].y); } }
;         float rstd[4];
; #pragma unroll
;         for (int r = 0; r < 4; ++r) { float ss = 0.f;
; #pragma unroll
;             for (int j = 0; j < 8; ++j) ss += (hv[r][j].x * hv[r][j].x + hv[r][j].y * hv[r][j].y) + (hv[r][j].z * hv[r][j].z + hv[r][j].w * hv[r][j].w);
;             rstd[r] = 1.f / sqrtf(wave_sum(ss) * (1.f / DM) + EPS_); }
	v_lshlrev_b32_e32 v14, 16, v174
	v_and_b32_e32 v15, 0xffff0000, v174
	v_pk_add_f32 v[152:153], v[10:11], v[14:15]
	v_cndmask_b32_e32 v14, v180, v182, vcc
	v_mov_b32_e32 v16, v157
	v_mov_b32_e32 v17, v147
	v_lshlrev_b32_e32 v193, 2, v14
	v_mov_b32_e32 v14, v156
	v_mov_b32_e32 v15, v146
	v_pk_mul_f32 v[16:17], v[16:17], v[16:17]
	v_mov_b32_e32 v18, v159
	v_mov_b32_e32 v19, v149
	v_pk_fma_f32 v[14:15], v[14:15], v[14:15], v[16:17]
	v_mov_b32_e32 v16, v158
	v_mov_b32_e32 v17, v148
	v_pk_mul_f32 v[18:19], v[18:19], v[18:19]
	v_mul_f32_e32 v20, v117, v117
	v_pk_fma_f32 v[16:17], v[16:17], v[16:17], v[18:19]
	v_mov_b32_e32 v18, v141
	v_mov_b32_e32 v19, v143
	v_pk_add_f32 v[14:15], v[14:15], v[16:17]
	v_mov_b32_e32 v16, v140
	v_mov_b32_e32 v17, v142
	v_pk_mul_f32 v[18:19], v[18:19], v[18:19]
	v_pk_add_f32 v[14:15], v[14:15], v[14:15] op_sel:[0,1] op_sel_hi:[1,0]
	v_pk_fma_f32 v[16:17], v[16:17], v[16:17], v[18:19]
	v_mul_f32_e32 v18, v105, v105
	v_pk_add_f32 v[16:17], v[16:17], v[16:17] op_sel:[0,1] op_sel_hi:[1,0]
	v_pk_fma_f32 v[18:19], v[104:105], v[104:105], v[18:19] op_sel_hi:[1,1,0]
	v_pk_fma_f32 v[20:21], v[116:117], v[116:117], v[20:21] op_sel_hi:[1,1,0]
	v_pk_mul_f32 v[22:23], v[96:97], v[96:97]
	v_pk_mul_f32 v[24:25], v[102:103], v[102:103]
	v_mov_b32_e32 v15, v22
	v_mov_b32_e32 v17, v23
	v_mov_b32_e32 v19, v24
	v_mov_b32_e32 v21, v25
	v_pk_add_f32 v[14:15], v[14:15], v[16:17]
	v_pk_add_f32 v[16:17], v[18:19], v[20:21]
	v_mov_b32_e32 v18, v91
	v_mov_b32_e32 v19, v93
	v_pk_add_f32 v[14:15], v[14:15], v[16:17]
	v_mov_b32_e32 v16, v90
	v_mov_b32_e32 v17, v92
	v_pk_mul_f32 v[18:19], v[18:19], v[18:19]
	v_mul_f32_e32 v20, v107, v107
	v_pk_fma_f32 v[16:17], v[16:17], v[16:17], v[18:19]
	v_mul_f32_e32 v18, v95, v95
	v_pk_add_f32 v[14:15], v[14:15], v[14:15] op_sel:[0,1] op_sel_hi:[1,0]
	v_pk_add_f32 v[16:17], v[16:17], v[16:17] op_sel:[0,1] op_sel_hi:[1,0]
	v_pk_fma_f32 v[18:19], v[94:95], v[94:95], v[18:19] op_sel_hi:[1,1,0]
	v_pk_fma_f32 v[20:21], v[106:107], v[106:107], v[20:21] op_sel_hi:[1,1,0]
	v_pk_mul_f32 v[22:23], v[114:115], v[114:115]
	v_pk_mul_f32 v[24:25], v[122:123], v[122:123]
	v_mov_b32_e32 v15, v22
	v_mov_b32_e32 v17, v23
	v_mov_b32_e32 v19, v24
	v_mov_b32_e32 v21, v25
	v_pk_add_f32 v[14:15], v[14:15], v[16:17]
	v_pk_add_f32 v[16:17], v[18:19], v[20:21]
	v_lshlrev_b32_e32 v10, 16, v175
	v_pk_add_f32 v[14:15], v[14:15], v[16:17]
	v_and_b32_e32 v11, 0xffff0000, v175
	v_add_f32_e32 v14, v14, v15
	ds_bpermute_b32 v15, v193, v14
	v_cmp_lt_i32_e32 vcc, v183, v181
	v_pk_add_f32 v[166:167], v[12:13], v[10:11]
	v_mov_b32_e32 v16, v163
	v_cndmask_b32_e32 v10, v180, v183, vcc
	v_lshlrev_b32_e32 v196, 2, v10
	s_waitcnt lgkmcnt(0)
	v_add_f32_e32 v11, v14, v15
	ds_bpermute_b32 v12, v196, v11
	v_cmp_lt_i32_e32 vcc, v184, v181
	s_waitcnt vmcnt(1)
	v_lshlrev_b32_e32 v10, 16, v44
	v_mov_b32_e32 v15, v151
	v_cndmask_b32_e32 v13, v180, v184, vcc
	v_lshlrev_b32_e32 v195, 2, v13
	s_waitcnt lgkmcnt(0)
	v_add_f32_e32 v12, v11, v12
	ds_bpermute_b32 v13, v195, v12
	v_cmp_lt_i32_e32 vcc, v185, v181
	v_and_b32_e32 v11, 0xffff0000, v44
	v_pk_add_f32 v[6:7], v[6:7], v[10:11]
	v_cndmask_b32_e32 v14, v180, v185, vcc
	v_lshlrev_b32_e32 v194, 2, v14
	s_waitcnt lgkmcnt(0)
	v_add_f32_e32 v12, v12, v13
	ds_bpermute_b32 v13, v194, v12
	v_cmp_lt_i32_e32 vcc, v186, v181
	v_mov_b32_e32 v14, v161
	v_pk_mul_f32 v[14:15], v[14:15], v[14:15]
	v_cndmask_b32_e32 v10, v180, v186, vcc
	v_lshlrev_b32_e32 v197, 2, v10
	s_waitcnt lgkmcnt(0)
	v_add_f32_e32 v11, v12, v13
	ds_bpermute_b32 v12, v197, v11
	v_cmp_lt_i32_e32 vcc, v187, v181
	v_mov_b32_e32 v17, v155
	v_pk_mul_f32 v[16:17], v[16:17], v[16:17]
	v_cndmask_b32_e32 v13, v180, v187, vcc
	v_lshlrev_b32_e32 v198, 2, v13
	s_waitcnt lgkmcnt(0)
	v_add_f32_e32 v12, v11, v12
	ds_bpermute_b32 v13, v198, v12
	v_mul_f32_e32 v18, v89, v89
	v_pk_fma_f32 v[18:19], v[88:89], v[88:89], v[18:19] op_sel_hi:[1,1,0]
	v_pk_mul_f32 v[20:21], v[78:79], v[78:79]
	v_pk_mul_f32 v[22:23], v[100:101], v[100:101]
	s_waitcnt lgkmcnt(0)
	v_add_f32_e32 v12, v12, v13
	v_fmamk_f32 v12, v12, 0x3a000000, v169
	v_mul_f32_e32 v13, 0x4f800000, v12
	v_cmp_gt_f32_e32 vcc, s47, v12
	v_mov_b32_e32 v19, v23
	v_lshlrev_b32_e32 v10, 16, v45
	v_cndmask_b32_e32 v24, v12, v13, vcc
	v_mov_b32_e32 v12, v160
	v_mov_b32_e32 v13, v150
	v_pk_fma_f32 v[12:13], v[12:13], v[12:13], v[14:15]
	v_mov_b32_e32 v14, v162
	v_mov_b32_e32 v15, v154
	v_pk_fma_f32 v[14:15], v[14:15], v[14:15], v[16:17]
	v_mov_b32_e32 v16, v129
	v_mov_b32_e32 v17, v145
	v_pk_add_f32 v[12:13], v[12:13], v[14:15]
	v_mov_b32_e32 v14, v128
	v_mov_b32_e32 v15, v144
	v_pk_mul_f32 v[16:17], v[16:17], v[16:17]
	v_pk_add_f32 v[12:13], v[12:13], v[12:13] op_sel:[0,1] op_sel_hi:[1,0]
	v_pk_fma_f32 v[14:15], v[14:15], v[14:15], v[16:17]
	v_mul_f32_e32 v16, v87, v87
	v_pk_add_f32 v[14:15], v[14:15], v[14:15] op_sel:[0,1] op_sel_hi:[1,0]
	v_pk_fma_f32 v[16:17], v[86:87], v[86:87], v[16:17] op_sel_hi:[1,1,0]
	v_mov_b32_e32 v13, v20
	v_mov_b32_e32 v15, v21
	v_mov_b32_e32 v17, v22
	v_pk_add_f32 v[12:13], v[12:13], v[14:15]
	v_pk_add_f32 v[14:15], v[16:17], v[18:19]
	v_mov_b32_e32 v16, v83
	v_mov_b32_e32 v17, v85
	v_pk_add_f32 v[12:13], v[12:13], v[14:15]
	v_mov_b32_e32 v14, v82
	v_mov_b32_e32 v15, v84
	v_pk_mul_f32 v[16:17], v[16:17], v[16:17]
	v_mul_f32_e32 v18, v109, v109
	v_pk_fma_f32 v[14:15], v[14:15], v[14:15], v[16:17]
	v_mul_f32_e32 v16, v99, v99
	v_pk_add_f32 v[12:13], v[12:13], v[12:13] op_sel:[0,1] op_sel_hi:[1,0]
	v_pk_add_f32 v[14:15], v[14:15], v[14:15] op_sel:[0,1] op_sel_hi:[1,0]
	v_pk_fma_f32 v[16:17], v[98:99], v[98:99], v[16:17] op_sel_hi:[1,1,0]
	v_pk_fma_f32 v[18:19], v[108:109], v[108:109], v[18:19] op_sel_hi:[1,1,0]
	v_pk_mul_f32 v[20:21], v[110:111], v[110:111]
	v_pk_mul_f32 v[22:23], v[124:125], v[124:125]
	v_mov_b32_e32 v13, v20
	v_mov_b32_e32 v15, v21
	v_mov_b32_e32 v17, v22
	v_mov_b32_e32 v19, v23
	v_pk_add_f32 v[12:13], v[12:13], v[14:15]
	v_pk_add_f32 v[14:15], v[16:17], v[18:19]
	v_sqrt_f32_e32 v25, v24
	v_pk_add_f32 v[12:13], v[12:13], v[14:15]
	v_and_b32_e32 v11, 0xffff0000, v45
	v_add_f32_e32 v12, v12, v13
	ds_bpermute_b32 v13, v193, v12
	v_pk_add_f32 v[8:9], v[8:9], v[10:11]
	s_waitcnt vmcnt(0)
; __device__ __forceinline__ void ph9_router(const Frame& F, const Args& A) {
;     ...
;             for (int j = 0; j < 8; ++j) { hv[r][j].x += bflo(dw[j].x); hv[r][j].y += bfhi(dw[j].x); hv[r][j].z += bflo(dw[j].y); hv[r][j].w += bfhi(dw[j].y); } }
;         float rstd[4];
; #pragma unroll
;         for (int r = 0; r < 4; ++r) { float ss = 0.f;
; #pragma unroll
;             for (int j = 0; j < 8; ++j) ss += (hv[r][j].x * hv[r][j].x + hv[r][j].y * hv[r][j].y) + (hv[r][j].z * hv[r][j].z + hv[r][j].w * hv[r][j].w);
;             rstd[r] = 1.f / sqrtf(wave_sum(ss) * (1.f / DM) + EPS_); }
	v_lshlrev_b32_e32 v10, 16, v42
	v_and_b32_e32 v11, 0xffff0000, v42
	v_pk_add_f32 v[2:3], v[2:3], v[10:11]
	s_waitcnt lgkmcnt(0)
	v_add_f32_e32 v12, v12, v13
	ds_bpermute_b32 v13, v196, v12
	v_add_u32_e32 v11, -1, v25
	v_fma_f32 v14, -v11, v25, v24
	v_cmp_ge_f32_e64 s[0:1], 0, v14
	v_add_u32_e32 v14, 1, v25
	s_waitcnt lgkmcnt(0)
	v_add_f32_e32 v12, v12, v13
	ds_bpermute_b32 v13, v195, v12
	v_fma_f32 v15, -v14, v25, v24
	v_cndmask_b32_e64 v11, v25, v11, s[0:1]
	v_cmp_lt_f32_e64 s[0:1], 0, v15
	v_lshlrev_b32_e32 v10, 16, v43
	s_waitcnt lgkmcnt(0)
	v_add_f32_e32 v12, v12, v13
	ds_bpermute_b32 v13, v194, v12
	v_cndmask_b32_e64 v11, v11, v14, s[0:1]
	v_mul_f32_e32 v14, 0x37800000, v11
	v_cndmask_b32_e32 v11, v11, v14, vcc
	v_cmp_class_f32_e32 vcc, v24, v171
	s_waitcnt lgkmcnt(0)
	v_add_f32_e32 v12, v12, v13
	ds_bpermute_b32 v13, v197, v12
	v_cndmask_b32_e32 v22, v11, v24, vcc
	v_div_scale_f32 v23, s[0:1], v22, v22, 1.0
	v_rcp_f32_e32 v24, v23
	v_and_b32_e32 v11, 0xffff0000, v43
	v_pk_add_f32 v[4:5], v[4:5], v[10:11]
	v_mov_b32_e32 v14, v69
	v_fma_f32 v10, -v23, v24, 1.0
	v_fmac_f32_e32 v24, v10, v24
	s_waitcnt lgkmcnt(0)
	v_add_f32_e32 v10, v12, v13
	ds_bpermute_b32 v11, v198, v10
	v_mov_b32_e32 v12, v73
	v_mov_b32_e32 v13, v63
	v_pk_mul_f32 v[12:13], v[12:13], v[12:13]
	v_mov_b32_e32 v15, v65
	s_waitcnt lgkmcnt(0)
	v_add_f32_e32 v10, v10, v11
	v_fmamk_f32 v10, v10, 0x3a000000, v169
	v_mul_f32_e32 v11, 0x4f800000, v10
	v_cmp_gt_f32_e64 s[0:1], s47, v10
	v_pk_mul_f32 v[14:15], v[14:15], v[14:15]
	v_mul_f32_e32 v16, v59, v59
	v_cndmask_b32_e64 v30, v10, v11, s[0:1]
	v_mov_b32_e32 v10, v72
	v_mov_b32_e32 v11, v62
	v_pk_fma_f32 v[10:11], v[10:11], v[10:11], v[12:13]
	v_mov_b32_e32 v12, v68
	v_mov_b32_e32 v13, v64
	v_pk_fma_f32 v[12:13], v[12:13], v[12:13], v[14:15]
	v_mov_b32_e32 v14, v55
	v_mov_b32_e32 v15, v57
	v_pk_add_f32 v[10:11], v[10:11], v[12:13]
	v_mov_b32_e32 v12, v54
	v_mov_b32_e32 v13, v56
	v_pk_mul_f32 v[14:15], v[14:15], v[14:15]
	v_pk_add_f32 v[10:11], v[10:11], v[10:11] op_sel:[0,1] op_sel_hi:[1,0]
	v_pk_fma_f32 v[12:13], v[12:13], v[12:13], v[14:15]
	v_mul_f32_e32 v14, v51, v51
	v_pk_add_f32 v[12:13], v[12:13], v[12:13] op_sel:[0,1] op_sel_hi:[1,0]
	v_pk_fma_f32 v[14:15], v[50:51], v[50:51], v[14:15] op_sel_hi:[1,1,0]
	v_pk_fma_f32 v[16:17], v[58:59], v[58:59], v[16:17] op_sel_hi:[1,1,0]
	v_pk_mul_f32 v[18:19], v[66:67], v[66:67]
	v_pk_mul_f32 v[20:21], v[70:71], v[70:71]
	v_mov_b32_e32 v11, v18
	v_mov_b32_e32 v13, v19
	v_mov_b32_e32 v15, v20
	v_mov_b32_e32 v17, v21
	v_pk_add_f32 v[10:11], v[10:11], v[12:13]
	v_pk_add_f32 v[12:13], v[14:15], v[16:17]
	v_mov_b32_e32 v14, v113
	v_mov_b32_e32 v15, v127
	v_pk_add_f32 v[10:11], v[10:11], v[12:13]
	v_mov_b32_e32 v12, v112
	v_mov_b32_e32 v13, v126
	v_pk_mul_f32 v[14:15], v[14:15], v[14:15]
	v_mul_f32_e32 v16, v121, v121
	v_pk_fma_f32 v[12:13], v[12:13], v[12:13], v[14:15]
	v_mul_f32_e32 v14, v119, v119
	v_pk_add_f32 v[10:11], v[10:11], v[10:11] op_sel:[0,1] op_sel_hi:[1,0]
	v_pk_add_f32 v[12:13], v[12:13], v[12:13] op_sel:[0,1] op_sel_hi:[1,0]
	v_pk_fma_f32 v[14:15], v[118:119], v[118:119], v[14:15] op_sel_hi:[1,1,0]
	v_pk_fma_f32 v[16:17], v[120:121], v[120:121], v[16:17] op_sel_hi:[1,1,0]
	v_pk_mul_f32 v[18:19], v[136:137], v[136:137]
	v_pk_mul_f32 v[20:21], v[138:139], v[138:139]
	v_mov_b32_e32 v11, v18
	v_mov_b32_e32 v13, v19
	v_mov_b32_e32 v15, v20
	v_mov_b32_e32 v17, v21
	v_pk_add_f32 v[10:11], v[10:11], v[12:13]
	v_pk_add_f32 v[12:13], v[14:15], v[16:17]
	v_sqrt_f32_e32 v31, v30
	v_pk_add_f32 v[10:11], v[10:11], v[12:13]
	v_div_scale_f32 v25, vcc, 1.0, v22, 1.0
	v_add_f32_e32 v10, v10, v11
	ds_bpermute_b32 v11, v193, v10
	v_add_u32_e32 v13, -1, v31
	v_fma_f32 v14, -v13, v31, v30
	v_cmp_ge_f32_e64 s[4:5], 0, v14
	v_add_u32_e32 v14, 1, v31
	s_waitcnt lgkmcnt(0)
	v_add_f32_e32 v10, v10, v11
	ds_bpermute_b32 v11, v196, v10
	v_fma_f32 v15, -v14, v31, v30
	v_cndmask_b32_e64 v13, v31, v13, s[4:5]
	v_cmp_lt_f32_e64 s[4:5], 0, v15
	v_mul_f32_e32 v26, v25, v24
	s_waitcnt lgkmcnt(0)
	v_add_f32_e32 v10, v10, v11
	ds_bpermute_b32 v11, v195, v10
	v_cndmask_b32_e64 v13, v13, v14, s[4:5]
	v_fma_f32 v27, -v23, v26, v25
	v_mul_f32_e32 v14, 0x37800000, v13
	v_fmac_f32_e32 v26, v27, v24
	s_waitcnt lgkmcnt(0)
	v_add_f32_e32 v10, v10, v11
	ds_bpermute_b32 v11, v194, v10
	v_cndmask_b32_e64 v13, v13, v14, s[0:1]
	v_cmp_class_f32_e64 s[0:1], v30, v171
	v_fma_f32 v12, -v23, v26, v25
	v_div_fmas_f32 v12, v12, v24, v26
	s_waitcnt lgkmcnt(0)
	v_add_f32_e32 v10, v10, v11
	ds_bpermute_b32 v11, v197, v10
	v_cndmask_b32_e64 v25, v13, v30, s[0:1]
	v_div_scale_f32 v27, s[0:1], v25, v25, 1.0
	v_rcp_f32_e32 v30, v27
	s_waitcnt lgkmcnt(0)
	v_add_f32_e32 v10, v10, v11
	ds_bpermute_b32 v11, v198, v10
	v_div_fixup_f32 v130, v12, v22, 1.0
	v_fma_f32 v12, -v27, v30, 1.0
	v_fmac_f32_e32 v30, v12, v30
	v_mov_b32_e32 v12, v39
	s_waitcnt lgkmcnt(0)
; __device__ __forceinline__ void ph9_router(const Frame& F, const Args& A) {
;     ...
;         float rstd[4];
; #pragma unroll
;         for (int r = 0; r < 4; ++r) { float ss = 0.f;
; #pragma unroll
;             for (int j = 0; j < 8; ++j) ss += (hv[r][j].x * hv[r][j].x + hv[r][j].y * hv[r][j].y) + (hv[r][j].z * hv[r][j].z + hv[r][j].w * hv[r][j].w);
;             rstd[r] = 1.f / sqrtf(wave_sum(ss) * (1.f / DM) + EPS_); }
; #pragma unroll
;         for (int j = 0; j < 8; ++j) { const int col = 4 * lane + 256 * j;
;             const f32x4 g = *(const f32x4*)(g2n + col), sh = *(const f32x4*)(MOD + 6144 + col), sc = *(const f32x4*)(MOD + 8192 + col);
;             const f32x4 gs1 = g * (sc + 1.f);
; #pragma unroll
;             for (int r = 0; r < 4; ++r) hv[r][j] = hv[r][j] * rstd[r] * gs1 + sh;
;             __builtin_amdgcn_sched_barrier(0); }
	v_add_f32_e32 v10, v10, v11
	v_fmamk_f32 v10, v10, 0x3a000000, v169
	v_mul_f32_e32 v11, 0x4f800000, v10
	v_cmp_gt_f32_e64 s[4:5], s47, v10
	v_mov_b32_e32 v13, v33
	v_pk_mul_f32 v[12:13], v[12:13], v[12:13]
	v_cndmask_b32_e64 v48, v10, v11, s[4:5]
	v_mov_b32_e32 v10, v38
	v_mov_b32_e32 v11, v32
	v_mov_b32_e32 v14, v41
	v_mov_b32_e32 v15, v29
	v_pk_fma_f32 v[10:11], v[10:11], v[10:11], v[12:13]
	v_mov_b32_e32 v12, v40
	v_mov_b32_e32 v13, v28
	v_pk_mul_f32 v[14:15], v[14:15], v[14:15]
	v_mul_f32_e32 v16, v61, v61
	v_pk_fma_f32 v[12:13], v[12:13], v[12:13], v[14:15]
	v_mov_b32_e32 v14, v35
	v_mov_b32_e32 v15, v37
	v_pk_add_f32 v[10:11], v[10:11], v[12:13]
	v_mov_b32_e32 v12, v34
	v_mov_b32_e32 v13, v36
	v_pk_mul_f32 v[14:15], v[14:15], v[14:15]
	v_pk_add_f32 v[10:11], v[10:11], v[10:11] op_sel:[0,1] op_sel_hi:[1,0]
	v_pk_fma_f32 v[12:13], v[12:13], v[12:13], v[14:15]
	v_mul_f32_e32 v14, v47, v47
	v_pk_add_f32 v[12:13], v[12:13], v[12:13] op_sel:[0,1] op_sel_hi:[1,0]
	v_pk_fma_f32 v[14:15], v[46:47], v[46:47], v[14:15] op_sel_hi:[1,1,0]
	v_pk_fma_f32 v[16:17], v[60:61], v[60:61], v[16:17] op_sel_hi:[1,1,0]
	v_pk_mul_f32 v[18:19], v[74:75], v[74:75]
	v_pk_mul_f32 v[20:21], v[164:165], v[164:165]
	v_mov_b32_e32 v11, v18
	v_mov_b32_e32 v13, v19
	v_mov_b32_e32 v15, v20
	v_mov_b32_e32 v17, v21
	v_pk_add_f32 v[10:11], v[10:11], v[12:13]
	v_pk_add_f32 v[12:13], v[14:15], v[16:17]
	v_mov_b32_e32 v14, v153
	v_mov_b32_e32 v15, v167
	v_pk_add_f32 v[10:11], v[10:11], v[12:13]
	v_mov_b32_e32 v12, v152
	v_mov_b32_e32 v13, v166
	v_pk_mul_f32 v[14:15], v[14:15], v[14:15]
	v_pk_add_f32 v[10:11], v[10:11], v[10:11] op_sel:[0,1] op_sel_hi:[1,0]
	v_pk_fma_f32 v[12:13], v[12:13], v[12:13], v[14:15]
	v_mul_f32_e32 v14, v7, v7
	v_pk_fma_f32 v[18:19], v[6:7], v[6:7], v[14:15] op_sel_hi:[1,1,0]
	v_mul_f32_e32 v14, v9, v9
	v_pk_add_f32 v[12:13], v[12:13], v[12:13] op_sel:[0,1] op_sel_hi:[1,0]
	v_pk_fma_f32 v[20:21], v[8:9], v[8:9], v[14:15] op_sel_hi:[1,1,0]
	v_pk_mul_f32 v[14:15], v[2:3], v[2:3]
	v_pk_mul_f32 v[16:17], v[4:5], v[4:5]
	v_mov_b32_e32 v11, v14
	v_mov_b32_e32 v13, v15
	v_pk_add_f32 v[22:23], v[10:11], v[12:13]
	v_lshlrev_b32_e32 v10, 2, v132
	v_ashrrev_i32_e32 v11, 31, v10
	v_lshlrev_b64 v[14:15], 2, v[10:11]
	v_lshl_add_u64 v[174:175], s[34:35], 0, v[14:15]
	v_lshl_add_u64 v[176:177], s[36:37], 0, v[14:15]
	global_load_dwordx4 v[42:45], v[174:175], off
	global_load_dwordx4 v[10:13], v[176:177], off
	v_lshl_add_u64 v[178:179], s[70:71], 0, v[14:15]
	v_mov_b32_e32 v19, v16
	v_mov_b32_e32 v21, v17
	global_load_dwordx4 v[14:17], v[178:179], off
	s_movk_i32 s98, 0x1000
	s_mov_b32 s99, 0
	global_load_dwordx4 v[200:203], v[176:177], off offset:1024
	global_load_dwordx4 v[204:207], v[178:179], off offset:1024
	global_load_dwordx4 v[208:211], v[174:175], off offset:1024
	global_load_dwordx4 v[212:215], v[176:177], off offset:2048
	global_load_dwordx4 v[216:219], v[178:179], off offset:2048
	global_load_dwordx4 v[220:223], v[174:175], off offset:2048
	global_load_dwordx4 v[224:227], v[176:177], off offset:3072
	global_load_dwordx4 v[228:231], v[178:179], off offset:3072
	global_load_dwordx4 v[232:235], v[174:175], off offset:3072
	v_lshl_add_u64 v[248:249], v[178:179], 0, s[98:99]
	v_lshl_add_u64 v[250:251], v[176:177], 0, s[98:99]
	v_lshl_add_u64 v[252:253], v[174:175], 0, s[98:99]
	global_load_dwordx4 v[236:239], v[248:249], off
	global_load_dwordx4 v[240:243], v[250:251], off
	global_load_dwordx4 v[244:247], v[252:253], off
	v_pk_add_f32 v[18:19], v[18:19], v[20:21]
	v_sqrt_f32_e32 v49, v48
	v_pk_add_f32 v[18:19], v[22:23], v[18:19]
	v_div_scale_f32 v24, vcc, 1.0, v25, 1.0
	v_add_f32_e32 v18, v18, v19
	ds_bpermute_b32 v19, v193, v18
	v_add_u32_e32 v21, -1, v49
	v_fma_f32 v22, -v21, v49, v48
	v_cmp_ge_f32_e64 s[0:1], 0, v22
	v_add_u32_e32 v22, 1, v49
	s_waitcnt lgkmcnt(0)
	v_add_f32_e32 v18, v18, v19
	ds_bpermute_b32 v19, v196, v18
	v_fma_f32 v23, -v22, v49, v48
	v_cndmask_b32_e64 v21, v49, v21, s[0:1]
	v_cmp_lt_f32_e64 s[0:1], 0, v23
	v_mul_f32_e32 v26, v24, v30
	s_waitcnt lgkmcnt(0)
	v_add_f32_e32 v18, v18, v19
	ds_bpermute_b32 v19, v195, v18
	v_cndmask_b32_e64 v21, v21, v22, s[0:1]
	v_mul_f32_e32 v22, 0x37800000, v21
	v_cndmask_b32_e64 v21, v21, v22, s[4:5]
	v_cmp_class_f32_e64 s[0:1], v48, v171
	s_waitcnt lgkmcnt(0)
	v_add_f32_e32 v18, v18, v19
	ds_bpermute_b32 v19, v194, v18
	v_cndmask_b32_e64 v21, v21, v48, s[0:1]
	v_div_scale_f32 v22, s[0:1], v21, v21, 1.0
	v_fma_f32 v31, -v27, v26, v24
	s_waitcnt lgkmcnt(0)
	v_add_f32_e32 v18, v18, v19
	ds_bpermute_b32 v19, v197, v18
	v_rcp_f32_e32 v23, v22
	v_fmac_f32_e32 v26, v31, v30
	v_fma_f32 v20, -v27, v26, v24
	v_div_fmas_f32 v20, v20, v30, v26
	s_waitcnt lgkmcnt(0)
	v_add_f32_e32 v18, v18, v19
	ds_bpermute_b32 v19, v198, v18
	v_div_fixup_f32 v168, v20, v25, 1.0
	v_fma_f32 v20, -v22, v23, 1.0
	v_fmac_f32_e32 v23, v20, v23
	v_div_scale_f32 v20, vcc, 1.0, v21, 1.0
	s_waitcnt lgkmcnt(0)
	v_add_f32_e32 v18, v18, v19
	v_fmamk_f32 v18, v18, 0x3a000000, v169
	v_mul_f32_e32 v19, 0x4f800000, v18
	v_cmp_gt_f32_e64 s[0:1], s47, v18
	v_mul_f32_e32 v24, v20, v23
	v_fma_f32 v25, -v22, v24, v20
	v_cndmask_b32_e64 v18, v18, v19, s[0:1]
	v_sqrt_f32_e32 v19, v18
	v_fmac_f32_e32 v24, v25, v23
	v_fma_f32 v20, -v22, v24, v20
	v_div_fmas_f32 v20, v20, v23, v24
	v_add_u32_e32 v22, -1, v19
	v_fma_f32 v25, -v22, v19, v18
	v_cmp_ge_f32_e64 s[4:5], 0, v25
	v_add_u32_e32 v25, 1, v19
	v_div_fixup_f32 v170, v20, v21, 1.0
	v_cndmask_b32_e64 v22, v19, v22, s[4:5]
	v_fma_f32 v19, -v25, v19, v18
	v_cmp_lt_f32_e64 s[4:5], 0, v19
	s_waitcnt vmcnt(13)
; __device__ __forceinline__ void ph9_router(const Frame& F, const Args& A) {
;     ...
;         for (int j = 0; j < 8; ++j) { const int col = 4 * lane + 256 * j;
;             const f32x4 g = *(const f32x4*)(g2n + col), sh = *(const f32x4*)(MOD + 6144 + col), sc = *(const f32x4*)(MOD + 8192 + col);
;             const f32x4 gs1 = g * (sc + 1.f);
; #pragma unroll
;             for (int r = 0; r < 4; ++r) hv[r][j] = hv[r][j] * rstd[r] * gs1 + sh;
;             __builtin_amdgcn_sched_barrier(0); }
	v_pk_add_f32 v[10:11], v[10:11], 1.0 op_sel_hi:[1,0]
	v_cndmask_b32_e64 v19, v22, v25, s[4:5]
	v_mul_f32_e32 v22, 0x37800000, v19
	v_cndmask_b32_e64 v19, v19, v22, s[0:1]
	v_cmp_class_f32_e64 s[0:1], v18, v171
	v_pk_add_f32 v[12:13], v[12:13], 1.0 op_sel_hi:[1,0]
	s_nop 0
	v_cndmask_b32_e64 v18, v19, v18, s[0:1]
	v_div_scale_f32 v19, s[0:1], v18, v18, 1.0
	v_rcp_f32_e32 v22, v19
	s_waitcnt vmcnt(12)
	v_pk_mul_f32 v[12:13], v[16:17], v[12:13]
	v_fma_f32 v20, -v19, v22, 1.0
	v_fmac_f32_e32 v22, v20, v22
	v_div_scale_f32 v20, vcc, 1.0, v18, 1.0
	v_mul_f32_e32 v21, v20, v22
	v_fma_f32 v23, -v19, v21, v20
	v_fmac_f32_e32 v21, v23, v22
	v_fma_f32 v19, -v19, v21, v20
	v_div_fmas_f32 v19, v19, v22, v21
	v_div_fixup_f32 v172, v19, v18, 1.0
	v_pk_mul_f32 v[18:19], v[14:15], v[10:11]
	v_pk_mul_f32 v[10:11], v[156:157], v[130:131] op_sel_hi:[1,0]
	v_pk_mul_f32 v[14:15], v[158:159], v[130:131] op_sel_hi:[1,0]
	v_pk_fma_f32 v[30:31], v[10:11], v[18:19], v[42:43]
	v_pk_mul_f32 v[10:11], v[160:161], v[168:169] op_sel_hi:[1,0]
	v_pk_fma_f32 v[26:27], v[14:15], v[12:13], v[44:45]
	v_pk_mul_f32 v[14:15], v[162:163], v[168:169] op_sel_hi:[1,0]
	v_pk_fma_f32 v[24:25], v[10:11], v[18:19], v[42:43]
	v_pk_mul_f32 v[10:11], v[72:73], v[170:171] op_sel_hi:[1,0]
	v_pk_fma_f32 v[20:21], v[14:15], v[12:13], v[44:45]
	v_pk_mul_f32 v[14:15], v[68:69], v[170:171] op_sel_hi:[1,0]
	v_pk_fma_f32 v[16:17], v[10:11], v[18:19], v[42:43]
	v_pk_mul_f32 v[22:23], v[38:39], v[172:173] op_sel_hi:[1,0]
	v_pk_mul_f32 v[10:11], v[40:41], v[172:173] op_sel_hi:[1,0]
	v_pk_fma_f32 v[14:15], v[14:15], v[12:13], v[44:45]
	v_pk_fma_f32 v[10:11], v[12:13], v[10:11], v[44:45]
	v_pk_fma_f32 v[12:13], v[18:19], v[22:23], v[42:43]
	s_waitcnt vmcnt(9)
	v_mov_b64_e32 v[38:39], v[200:201]
	v_mov_b64_e32 v[40:41], v[202:203]
	v_mov_b64_e32 v[42:43], v[204:205]
	v_mov_b64_e32 v[44:45], v[206:207]
	v_mov_b64_e32 v[156:157], v[208:209]
	v_mov_b64_e32 v[158:159], v[210:211]
	global_load_dwordx4 v[200:203], v[250:251], off offset:1024
	global_load_dwordx4 v[204:207], v[248:249], off offset:1024
	global_load_dwordx4 v[208:211], v[252:253], off offset:1024
	v_pk_mul_f32 v[76:77], v[32:33], v[172:173] op_sel_hi:[1,0]
	v_pk_mul_f32 v[80:81], v[28:29], v[172:173] op_sel_hi:[1,0]
	v_pk_mul_f32 v[18:19], v[146:147], v[130:131] op_sel_hi:[1,0]
	v_pk_mul_f32 v[22:23], v[148:149], v[130:131] op_sel_hi:[1,0]
	v_pk_mul_f32 v[68:69], v[150:151], v[168:169] op_sel_hi:[1,0]
	v_pk_mul_f32 v[72:73], v[154:155], v[168:169] op_sel_hi:[1,0]
	v_pk_mul_f32 v[62:63], v[62:63], v[170:171] op_sel_hi:[1,0]
	v_pk_mul_f32 v[64:65], v[64:65], v[170:171] op_sel_hi:[1,0]
	v_pk_add_f32 v[28:29], v[40:41], 1.0 op_sel_hi:[1,0]
	v_pk_add_f32 v[32:33], v[38:39], 1.0 op_sel_hi:[1,0]
	v_pk_mul_f32 v[44:45], v[44:45], v[28:29]
	v_pk_mul_f32 v[42:43], v[42:43], v[32:33]
	v_pk_fma_f32 v[48:49], v[22:23], v[44:45], v[158:159]
	v_pk_fma_f32 v[52:53], v[18:19], v[42:43], v[156:157]
	v_pk_fma_f32 v[38:39], v[72:73], v[44:45], v[158:159]
	v_pk_fma_f32 v[40:41], v[68:69], v[42:43], v[156:157]
	v_pk_fma_f32 v[28:29], v[64:65], v[44:45], v[158:159]
	v_pk_fma_f32 v[32:33], v[62:63], v[42:43], v[156:157]
	v_pk_fma_f32 v[18:19], v[80:81], v[44:45], v[158:159]
	v_pk_fma_f32 v[22:23], v[76:77], v[42:43], v[156:157]
	s_waitcnt vmcnt(9)
	v_mov_b64_e32 v[42:43], v[212:213]
	v_mov_b64_e32 v[44:45], v[214:215]
	v_mov_b64_e32 v[62:63], v[216:217]
	v_mov_b64_e32 v[64:65], v[218:219]
	v_mov_b64_e32 v[146:147], v[220:221]
	v_mov_b64_e32 v[148:149], v[222:223]
	global_load_dwordx4 v[212:215], v[250:251], off offset:2048
	global_load_dwordx4 v[216:219], v[248:249], off offset:2048
	global_load_dwordx4 v[220:223], v[252:253], off offset:2048
	v_pk_mul_f32 v[72:73], v[142:143], v[130:131] op_sel_hi:[1,0]
	v_pk_mul_f32 v[142:143], v[34:35], v[172:173] op_sel_hi:[1,0]
	v_pk_mul_f32 v[34:35], v[36:37], v[172:173] op_sel_hi:[1,0]
	v_pk_mul_f32 v[68:69], v[140:141], v[130:131] op_sel_hi:[1,0]
	v_pk_mul_f32 v[76:77], v[128:129], v[168:169] op_sel_hi:[1,0]
	v_pk_mul_f32 v[80:81], v[144:145], v[168:169] op_sel_hi:[1,0]
	v_pk_mul_f32 v[128:129], v[54:55], v[170:171] op_sel_hi:[1,0]
	v_pk_mul_f32 v[140:141], v[56:57], v[170:171] op_sel_hi:[1,0]
	v_pk_add_f32 v[36:37], v[44:45], 1.0 op_sel_hi:[1,0]
	v_pk_add_f32 v[42:43], v[42:43], 1.0 op_sel_hi:[1,0]
	v_pk_mul_f32 v[36:37], v[64:65], v[36:37]
	v_pk_mul_f32 v[144:145], v[62:63], v[42:43]
	v_pk_fma_f32 v[62:63], v[72:73], v[36:37], v[148:149]
	v_pk_fma_f32 v[64:65], v[68:69], v[144:145], v[146:147]
	v_pk_fma_f32 v[54:55], v[80:81], v[36:37], v[148:149]
	v_pk_fma_f32 v[56:57], v[76:77], v[144:145], v[146:147]
	v_pk_fma_f32 v[42:43], v[140:141], v[36:37], v[148:149]
	v_pk_fma_f32 v[44:45], v[128:129], v[144:145], v[146:147]
	v_pk_fma_f32 v[34:35], v[34:35], v[36:37], v[148:149]
	v_pk_fma_f32 v[36:37], v[142:143], v[144:145], v[146:147]
	s_waitcnt vmcnt(9)
; __device__ __forceinline__ void ph9_router(const Frame& F, const Args& A) {
;     ...
;         for (int j = 0; j < 8; ++j) { const int col = 4 * lane + 256 * j;
;             const f32x4 g = *(const f32x4*)(g2n + col), sh = *(const f32x4*)(MOD + 6144 + col), sc = *(const f32x4*)(MOD + 8192 + col);
;             const f32x4 gs1 = g * (sc + 1.f);
; #pragma unroll
;             for (int r = 0; r < 4; ++r) hv[r][j] = hv[r][j] * rstd[r] * gs1 + sh;
;             __builtin_amdgcn_sched_barrier(0); }
	v_mov_b64_e32 v[140:141], v[224:225]
	v_mov_b64_e32 v[142:143], v[226:227]
	v_mov_b64_e32 v[144:145], v[228:229]
	v_mov_b64_e32 v[146:147], v[230:231]
	v_mov_b64_e32 v[148:149], v[232:233]
	v_mov_b64_e32 v[150:151], v[234:235]
	global_load_dwordx4 v[224:227], v[250:251], off offset:3072
	global_load_dwordx4 v[228:231], v[248:249], off offset:3072
	global_load_dwordx4 v[232:235], v[252:253], off offset:3072
	v_pk_mul_f32 v[68:69], v[104:105], v[130:131] op_sel_hi:[1,0]
	v_pk_mul_f32 v[104:105], v[46:47], v[172:173] op_sel_hi:[1,0]
	v_pk_mul_f32 v[46:47], v[60:61], v[172:173] op_sel_hi:[1,0]
	v_pk_mul_f32 v[72:73], v[116:117], v[130:131] op_sel_hi:[1,0]
	v_pk_mul_f32 v[86:87], v[86:87], v[168:169] op_sel_hi:[1,0]
	v_pk_mul_f32 v[88:89], v[88:89], v[168:169] op_sel_hi:[1,0]
	v_pk_mul_f32 v[50:51], v[50:51], v[170:171] op_sel_hi:[1,0]
	v_pk_mul_f32 v[58:59], v[58:59], v[170:171] op_sel_hi:[1,0]
	v_pk_add_f32 v[60:61], v[142:143], 1.0 op_sel_hi:[1,0]
	v_pk_add_f32 v[76:77], v[140:141], 1.0 op_sel_hi:[1,0]
	v_pk_mul_f32 v[116:117], v[146:147], v[60:61]
	v_pk_mul_f32 v[128:129], v[144:145], v[76:77]
	v_pk_fma_f32 v[76:77], v[72:73], v[116:117], v[150:151]
	v_pk_fma_f32 v[80:81], v[68:69], v[128:129], v[148:149]
	v_pk_fma_f32 v[68:69], v[88:89], v[116:117], v[150:151]
	v_pk_fma_f32 v[72:73], v[86:87], v[128:129], v[148:149]
	v_pk_fma_f32 v[58:59], v[58:59], v[116:117], v[150:151]
	v_pk_fma_f32 v[60:61], v[50:51], v[128:129], v[148:149]
	v_pk_fma_f32 v[46:47], v[46:47], v[116:117], v[150:151]
	v_pk_fma_f32 v[50:51], v[104:105], v[128:129], v[148:149]
	v_add_co_u32_e32 v148, vcc, s46, v178
	v_pk_mul_f32 v[104:105], v[96:97], v[130:131] op_sel_hi:[1,0]
	s_nop 0
	v_addc_co_u32_e32 v149, vcc, 0, v179, vcc
	v_add_co_u32_e32 v150, vcc, s46, v176
	s_waitcnt vmcnt(9)
	v_mov_b64_e32 v[86:87], v[236:237]
	v_mov_b64_e32 v[88:89], v[238:239]
	s_nop 0
	v_addc_co_u32_e32 v151, vcc, 0, v177, vcc
	v_mov_b64_e32 v[140:141], v[240:241]
	v_mov_b64_e32 v[142:143], v[242:243]
	v_add_co_u32_e32 v154, vcc, s46, v174
	v_pk_mul_f32 v[96:97], v[102:103], v[130:131] op_sel_hi:[1,0]
	s_nop 0
	v_addc_co_u32_e32 v155, vcc, 0, v175, vcc
	v_mov_b64_e32 v[144:145], v[244:245]
	v_mov_b64_e32 v[146:147], v[246:247]
	v_pk_mul_f32 v[102:103], v[100:101], v[168:169] op_sel_hi:[1,0]
	v_pk_mul_f32 v[116:117], v[74:75], v[172:173] op_sel_hi:[1,0]
	v_pk_mul_f32 v[78:79], v[78:79], v[168:169] op_sel_hi:[1,0]
	v_pk_mul_f32 v[66:67], v[66:67], v[170:171] op_sel_hi:[1,0]
	v_pk_mul_f32 v[70:71], v[70:71], v[170:171] op_sel_hi:[1,0]
	v_pk_mul_f32 v[128:129], v[164:165], v[172:173] op_sel_hi:[1,0]
	v_pk_add_f32 v[74:75], v[142:143], 1.0 op_sel_hi:[1,0]
	v_pk_add_f32 v[100:101], v[140:141], 1.0 op_sel_hi:[1,0]
	v_pk_mul_f32 v[140:141], v[88:89], v[74:75]
	v_pk_mul_f32 v[142:143], v[86:87], v[100:101]
	v_pk_fma_f32 v[96:97], v[96:97], v[140:141], v[146:147]
	v_pk_fma_f32 v[100:101], v[104:105], v[142:143], v[144:145]
	v_pk_fma_f32 v[86:87], v[102:103], v[140:141], v[146:147]
	v_pk_fma_f32 v[88:89], v[78:79], v[142:143], v[144:145]
	v_pk_fma_f32 v[74:75], v[70:71], v[140:141], v[146:147]
	v_pk_fma_f32 v[78:79], v[66:67], v[142:143], v[144:145]
	v_pk_fma_f32 v[66:67], v[128:129], v[140:141], v[146:147]
	v_pk_fma_f32 v[70:71], v[116:117], v[142:143], v[144:145]
	s_waitcnt vmcnt(6)
	v_mov_b64_e32 v[102:103], v[200:201]
	v_mov_b64_e32 v[104:105], v[202:203]
	v_mov_b64_e32 v[140:141], v[204:205]
	v_mov_b64_e32 v[142:143], v[206:207]
	v_mov_b64_e32 v[144:145], v[208:209]
	v_mov_b64_e32 v[146:147], v[210:211]
	v_pk_mul_f32 v[90:91], v[90:91], v[130:131] op_sel_hi:[1,0]
	v_pk_mul_f32 v[92:93], v[92:93], v[130:131] op_sel_hi:[1,0]
	v_pk_mul_f32 v[82:83], v[82:83], v[168:169] op_sel_hi:[1,0]
	v_pk_mul_f32 v[84:85], v[84:85], v[168:169] op_sel_hi:[1,0]
	v_pk_mul_f32 v[128:129], v[112:113], v[170:171] op_sel_hi:[1,0]
	v_pk_mul_f32 v[126:127], v[126:127], v[170:171] op_sel_hi:[1,0]
	v_pk_mul_f32 v[152:153], v[152:153], v[172:173] op_sel_hi:[1,0]
	v_pk_mul_f32 v[156:157], v[166:167], v[172:173] op_sel_hi:[1,0]
	v_pk_add_f32 v[104:105], v[104:105], 1.0 op_sel_hi:[1,0]
	v_pk_add_f32 v[102:103], v[102:103], 1.0 op_sel_hi:[1,0]
	v_pk_mul_f32 v[142:143], v[142:143], v[104:105]
	v_pk_mul_f32 v[140:141], v[140:141], v[102:103]
	v_pk_fma_f32 v[112:113], v[92:93], v[142:143], v[146:147]
	v_pk_fma_f32 v[116:117], v[90:91], v[140:141], v[144:145]
	v_pk_fma_f32 v[102:103], v[84:85], v[142:143], v[146:147]
	v_pk_fma_f32 v[104:105], v[82:83], v[140:141], v[144:145]
	v_pk_fma_f32 v[90:91], v[126:127], v[142:143], v[146:147]
	v_pk_fma_f32 v[92:93], v[128:129], v[140:141], v[144:145]
	v_pk_fma_f32 v[82:83], v[156:157], v[142:143], v[146:147]
	v_pk_fma_f32 v[84:85], v[152:153], v[140:141], v[144:145]
	s_waitcnt vmcnt(3)
; __device__ __forceinline__ void ph9_router(const Frame& F, const Args& A) {
;     ...
;         for (int j = 0; j < 8; ++j) { const int col = 4 * lane + 256 * j;
;             const f32x4 g = *(const f32x4*)(g2n + col), sh = *(const f32x4*)(MOD + 6144 + col), sc = *(const f32x4*)(MOD + 8192 + col);
;             const f32x4 gs1 = g * (sc + 1.f);
; #pragma unroll
;             for (int r = 0; r < 4; ++r) hv[r][j] = hv[r][j] * rstd[r] * gs1 + sh;
;             __builtin_amdgcn_sched_barrier(0); }
;         float lgv[2];
; #pragma unroll 1
;         for (int half = 0; half < 2; ++half) {
;             if (half == 1) { __syncthreads();
;               const f32x4* src = (const f32x4*)(WRT + (size_t)16 * DM);
; #pragma unroll 1
;               for (int i0 = 0; i0 < 16; i0 += 8) { f32x4 t8[8];
; #pragma unroll
;                 for (int i = 0; i < 8; ++i) t8[i] = src[tid + 512 * (i0 + i)];
; #pragma unroll
;                 for (int i = 0; i < 8; ++i) wl[tid + 512 * (i0 + i)] = t8[i]; } }
	v_mov_b64_e32 v[126:127], v[212:213]
	v_mov_b64_e32 v[128:129], v[214:215]
	v_mov_b64_e32 v[140:141], v[216:217]
	v_mov_b64_e32 v[142:143], v[218:219]
	v_mov_b64_e32 v[144:145], v[220:221]
	v_mov_b64_e32 v[146:147], v[222:223]
	v_pk_mul_f32 v[152:153], v[118:119], v[170:171] op_sel_hi:[1,0]
	v_pk_mul_f32 v[156:157], v[120:121], v[170:171] op_sel_hi:[1,0]
	v_pk_mul_f32 v[94:95], v[94:95], v[130:131] op_sel_hi:[1,0]
	v_pk_mul_f32 v[106:107], v[106:107], v[130:131] op_sel_hi:[1,0]
	v_pk_mul_f32 v[98:99], v[98:99], v[168:169] op_sel_hi:[1,0]
	v_pk_mul_f32 v[108:109], v[108:109], v[168:169] op_sel_hi:[1,0]
	v_pk_mul_f32 v[6:7], v[6:7], v[172:173] op_sel_hi:[1,0]
	v_pk_mul_f32 v[8:9], v[8:9], v[172:173] op_sel_hi:[1,0]
	v_pk_add_f32 v[118:119], v[128:129], 1.0 op_sel_hi:[1,0]
	v_pk_add_f32 v[120:121], v[126:127], 1.0 op_sel_hi:[1,0]
	v_pk_mul_f32 v[142:143], v[142:143], v[118:119]
	v_pk_mul_f32 v[140:141], v[140:141], v[120:121]
	v_pk_fma_f32 v[126:127], v[106:107], v[142:143], v[146:147]
	v_pk_fma_f32 v[128:129], v[94:95], v[140:141], v[144:145]
	v_pk_fma_f32 v[118:119], v[108:109], v[142:143], v[146:147]
	v_pk_fma_f32 v[120:121], v[98:99], v[140:141], v[144:145]
	v_pk_fma_f32 v[106:107], v[156:157], v[142:143], v[146:147]
	v_pk_fma_f32 v[108:109], v[152:153], v[140:141], v[144:145]
	v_pk_fma_f32 v[94:95], v[8:9], v[142:143], v[146:147]
	v_pk_fma_f32 v[98:99], v[6:7], v[140:141], v[144:145]
	s_waitcnt vmcnt(0)
	v_mov_b64_e32 v[6:7], v[224:225]
	v_mov_b64_e32 v[8:9], v[226:227]
	v_mov_b64_e32 v[140:141], v[228:229]
	v_mov_b64_e32 v[142:143], v[230:231]
	v_mov_b64_e32 v[144:145], v[232:233]
	v_mov_b64_e32 v[146:147], v[234:235]
	v_pk_mul_f32 v[114:115], v[114:115], v[130:131] op_sel_hi:[1,0]
	v_pk_mul_f32 v[122:123], v[122:123], v[130:131] op_sel_hi:[1,0]
	v_pk_mul_f32 v[110:111], v[110:111], v[168:169] op_sel_hi:[1,0]
	v_pk_mul_f32 v[124:125], v[124:125], v[168:169] op_sel_hi:[1,0]
	v_pk_mul_f32 v[148:149], v[136:137], v[170:171] op_sel_hi:[1,0]
	v_pk_mul_f32 v[150:151], v[138:139], v[170:171] op_sel_hi:[1,0]
	v_pk_mul_f32 v[2:3], v[2:3], v[172:173] op_sel_hi:[1,0]
	v_pk_mul_f32 v[4:5], v[4:5], v[172:173] op_sel_hi:[1,0]
	v_pk_add_f32 v[8:9], v[8:9], 1.0 op_sel_hi:[1,0]
	v_pk_add_f32 v[6:7], v[6:7], 1.0 op_sel_hi:[1,0]
	v_pk_mul_f32 v[8:9], v[142:143], v[8:9]
	v_pk_mul_f32 v[6:7], v[140:141], v[6:7]
	v_pk_fma_f32 v[140:141], v[122:123], v[8:9], v[146:147]
	v_pk_fma_f32 v[142:143], v[114:115], v[6:7], v[144:145]
	v_pk_fma_f32 v[136:137], v[124:125], v[8:9], v[146:147]
	v_pk_fma_f32 v[138:139], v[110:111], v[6:7], v[144:145]
	v_pk_fma_f32 v[122:123], v[150:151], v[8:9], v[146:147]
	v_pk_fma_f32 v[124:125], v[148:149], v[6:7], v[144:145]
	v_pk_fma_f32 v[110:111], v[4:5], v[8:9], v[146:147]
	v_pk_fma_f32 v[114:115], v[2:3], v[6:7], v[144:145]
	v_and_b32_e32 v2, 1, v132
	v_cmp_eq_u32_e64 s[4:5], 0, v2
	v_and_b32_e32 v2, 2, v132
	v_cmp_eq_u32_e64 s[6:7], 0, v2
	v_and_b32_e32 v2, 16, v132
	v_cmp_eq_u32_e64 s[8:9], 0, v2
	v_and_b32_e32 v2, 32, v132
	v_cmp_eq_u32_e64 s[10:11], 0, v2
	v_lshlrev_b32_e32 v2, 13, v132
	v_lshl_add_u32 v157, v132, 4, 0
	v_and_b32_e32 v156, 15, v132
	v_and_b32_e32 v158, 0x18000, v2
	s_mov_b64 s[0:1], -1
	s_mov_b64 s[12:13], 0
	s_mov_b32 s98, s38
	s_mov_b32 s99, s39
	global_load_dwordx4 v[200:203], v135, s[98:99]
	s_add_u32 s98, s98, 0x2000
	s_addc_u32 s99, s99, 0
	global_load_dwordx4 v[204:207], v135, s[98:99]
	s_add_u32 s98, s98, 0x2000
	s_addc_u32 s99, s99, 0
	global_load_dwordx4 v[208:211], v135, s[98:99]
	s_add_u32 s98, s98, 0x2000
	s_addc_u32 s99, s99, 0
	global_load_dwordx4 v[212:215], v135, s[98:99]
	s_add_u32 s98, s98, 0x2000
	s_addc_u32 s99, s99, 0
	global_load_dwordx4 v[216:219], v135, s[98:99]
	s_add_u32 s98, s98, 0x2000
	s_addc_u32 s99, s99, 0
	global_load_dwordx4 v[220:223], v135, s[98:99]
	s_add_u32 s98, s98, 0x2000
	s_addc_u32 s99, s99, 0
	global_load_dwordx4 v[224:227], v135, s[98:99]
	s_add_u32 s98, s98, 0x2000
	s_addc_u32 s99, s99, 0
	global_load_dwordx4 v[234:237], v135, s[98:99]
	s_add_u32 s98, s98, 0x2000
	s_addc_u32 s99, s99, 0
	global_load_dwordx4 v[238:241], v135, s[98:99]
	s_add_u32 s98, s98, 0x2000
	s_addc_u32 s99, s99, 0
	global_load_dwordx4 v[242:245], v135, s[98:99]
	s_add_u32 s98, s98, 0x2000
	s_addc_u32 s99, s99, 0
	global_load_dwordx4 v[246:249], v135, s[98:99]
	s_add_u32 s98, s98, 0x2000
	s_addc_u32 s99, s99, 0
	global_load_dwordx4 v[250:253], v135, s[98:99]
	s_cbranch_execnz .LBB0_1198
.LBB0_1196:
	s_add_u32 s98, s38, 0x18000
	s_addc_u32 s99, s39, 0
	global_load_dwordx4 v[2:5], v135, s[98:99]
	s_add_u32 s98, s98, 0x2000
	s_addc_u32 s99, s99, 0
	global_load_dwordx4 v[6:9], v135, s[98:99]
	s_add_u32 s98, s98, 0x2000
	s_addc_u32 s99, s99, 0
	global_load_dwordx4 v[144:147], v135, s[98:99]
	s_add_u32 s98, s98, 0x2000
	s_addc_u32 s99, s99, 0
	global_load_dwordx4 v[148:151], v135, s[98:99]
	v_add_u32_e32 v130, 0x10000, v135
	s_mov_b32 s33, 8
	s_mov_b64 s[14:15], 0
	s_barrier
	s_waitcnt vmcnt(4)
	ds_write_b128 v135, v[200:203]
	ds_write_b128 v135, v[204:207] offset:8192
	ds_write_b128 v135, v[208:211] offset:16384
	ds_write_b128 v135, v[212:215] offset:24576
	ds_write_b128 v135, v[216:219] offset:32768
	ds_write_b128 v135, v[220:223] offset:40960
	ds_write_b128 v135, v[224:227] offset:49152
	ds_write_b128 v135, v[234:237] offset:57344
	ds_write_b128 v130, v[238:241]
	ds_write_b128 v130, v[242:245] offset:8192
	ds_write_b128 v130, v[246:249] offset:16384
	ds_write_b128 v130, v[250:253] offset:24576
	s_waitcnt vmcnt(0)
	ds_write_b128 v130, v[2:5] offset:32768
	ds_write_b128 v130, v[6:9] offset:40960
	ds_write_b128 v130, v[144:147] offset:49152
	ds_write_b128 v130, v[148:151] offset:57344
